# sliding-window attention: K/Q fragment loads issued lane-transposed (coalesced 64-B per lane quad) + ds_bpermute back to MFMA operand layout
# baseline (speedup 1.0000x reference)
; #define MFMA16(a, b, c) __builtin_amdgcn_mfma_f32_16x16x32_bf16(a, b, c, 0, 0, 0)
; __device__ __forceinline__ void swa_phase(const Ctx& C, const bf16* PROJ, const float* sinks, bf16* YSWA) {
;     ...
;             const int h = 3 * hk + g; const float sink2 = sinks[h] * LOG2E;
;             const int q0 = tb + 16 * w;
;             f32x4 s[9];
; #pragma unroll
;             for (int j = 0; j < 9; ++j) { f32x4 a = {0.f, 0.f, 0.f, 0.f}; a = MFMA16(kf[j][0], qf[g][0], a); a = MFMA16(kf[j][1], qf[g][1], a); s[j] = a; }
;             const int qr = 16 * w + c16; float mx = -INFINITY;
; #pragma unroll
;             for (int j = 0; j < 9; ++j)
; #pragma unroll
;                 for (int r = 0; r < 4; ++r) { const int kr = 16 * w - 128 + 16 * j + 4 * g4 + r, diff = qr - kr; const bool ok = diff >= 0 && diff < 128 && (128 * n + kr) >= 0;
;                     s[j][r] = ok ? s[j][r] : -INFINITY; mx = fmaxf(mx, s[j][r]); }
;             mx = fmaxf(mx, __shfl_xor(mx, 16)); mx = fmaxf(mx, __shfl_xor(mx, 32)); mx = fmaxf(mx, sink2);
.LBB0_527:
	s_nop 0
	v_readlane_b32 s0, v255, 7
	s_cmp_lt_i32 s0, 2
	s_mov_b64 s[0:1], -1
	s_cbranch_scc1 .LBB0_538
	v_readlane_b32 s0, v255, 7
	s_cmp_lt_i32 s0, 3
	s_cbranch_scc0 .LBB0_537
	v_readlane_b32 s0, v254, 47
	v_readlane_b32 s1, v254, 48
	s_andn2_b64 vcc, exec, s[0:1]
	s_barrier
	s_cbranch_vccnz .LBB0_536
	v_readlane_b32 s0, v254, 30
	v_readlane_b32 s1, v254, 31
	s_load_dwordx2 s[0:1], s[0:1], 0x50
	s_waitcnt vmcnt(6)
	v_and_b32_e32 v6, 64, v215
	v_xor_b32_e32 v5, 16, v215
	v_add_u32_e32 v6, 64, v6
	v_ashrrev_i32_e32 v1, 4, v175
	v_readlane_b32 s2, v255, 3
	v_cmp_lt_i32_e32 vcc, v5, v6
	v_and_b32_e32 v3, 15, v175
	v_readlane_b32 s16, v254, 18
	v_lshlrev_b32_e32 v0, 2, v1
	s_waitcnt lgkmcnt(0)
	s_add_u32 s36, s0, s2
	v_readlane_b32 s0, v253, 59
	v_cndmask_b32_e32 v7, v215, v5, vcc
	v_xor_b32_e32 v5, 32, v215
	v_or_b32_e32 v182, s16, v3
	v_readlane_b32 s3, v255, 4
	v_add_u32_e32 v4, s0, v0
	v_cmp_lt_i32_e32 vcc, v5, v6
	s_addc_u32 s37, s1, s3
	s_movk_i32 s1, 0x80
	v_cndmask_b32_e32 v6, v215, v5, vcc
	v_sub_u32_e32 v5, v182, v4
	v_readlane_b32 s14, v254, 53
	v_cmp_gt_u32_e32 vcc, s1, v5
	v_sub_u32_e32 v5, v4, v182
	v_cmp_lt_i32_e64 s[2:3], s14, v4
	s_movk_i32 s0, 0xff7f
	s_and_b64 s[40:41], vcc, s[2:3]
	v_cmp_lt_u32_e32 vcc, s0, v5
	v_or_b32_e32 v5, 2, v4
	v_cmp_le_i32_e64 s[2:3], s14, v4
	s_waitcnt vmcnt(5)
	v_sub_u32_e32 v9, v182, v5
	s_and_b64 s[42:43], vcc, s[2:3]
	v_cmp_gt_u32_e32 vcc, s1, v9
	v_cmp_lt_i32_e64 s[2:3], s14, v5
	v_or_b32_e32 v5, 3, v4
	s_and_b64 s[44:45], vcc, s[2:3]
	v_sub_u32_e32 v9, v182, v5
	v_cmp_lt_i32_e64 s[2:3], s14, v5
	v_add_u32_e32 v5, 16, v4
	v_cmp_gt_u32_e32 vcc, s1, v9
	v_sub_u32_e32 v9, v182, v5
	s_and_b64 s[46:47], vcc, s[2:3]
	v_cmp_gt_u32_e32 vcc, s1, v9
	v_cmp_lt_i32_e64 s[2:3], s14, v5
	v_add_u32_e32 v5, 17, v4
	s_and_b64 s[48:49], vcc, s[2:3]
	v_sub_u32_e32 v9, v182, v5
	v_cmp_lt_i32_e64 s[2:3], s14, v5
	v_add_u32_e32 v5, 18, v4
	v_cmp_gt_u32_e32 vcc, s1, v9
	v_sub_u32_e32 v9, v182, v5
	s_and_b64 s[50:51], vcc, s[2:3]
	v_cmp_gt_u32_e32 vcc, s1, v9
	v_cmp_lt_i32_e64 s[2:3], s14, v5
	v_add_u32_e32 v5, 19, v4
	s_and_b64 s[52:53], vcc, s[2:3]
	v_sub_u32_e32 v9, v182, v5
	v_cmp_lt_i32_e64 s[2:3], s14, v5
	v_add_u32_e32 v5, 32, v4
	v_cmp_gt_u32_e32 vcc, s1, v9
	v_sub_u32_e32 v9, v182, v5
	s_and_b64 s[54:55], vcc, s[2:3]
	v_cmp_gt_u32_e32 vcc, s1, v9
	v_cmp_lt_i32_e64 s[2:3], s14, v5
	v_add_u32_e32 v5, 33, v4
	s_and_b64 s[56:57], vcc, s[2:3]
	v_sub_u32_e32 v9, v182, v5
	v_cmp_lt_i32_e64 s[2:3], s14, v5
	v_add_u32_e32 v5, 34, v4
	v_cmp_gt_u32_e32 vcc, s1, v9
	v_sub_u32_e32 v9, v182, v5
	s_and_b64 s[58:59], vcc, s[2:3]
	v_cmp_gt_u32_e32 vcc, s1, v9
	v_cmp_lt_i32_e64 s[2:3], s14, v5
	v_add_u32_e32 v5, 35, v4
	s_and_b64 s[60:61], vcc, s[2:3]
	v_sub_u32_e32 v9, v182, v5
	v_cmp_lt_i32_e64 s[2:3], s14, v5
	v_add_u32_e32 v5, 48, v4
	v_cmp_gt_u32_e32 vcc, s1, v9
	v_sub_u32_e32 v9, v182, v5
	s_and_b64 s[62:63], vcc, s[2:3]
	v_cmp_gt_u32_e32 vcc, s1, v9
	v_cmp_lt_i32_e64 s[2:3], s14, v5
	v_add_u32_e32 v5, 49, v4
	s_and_b64 s[64:65], vcc, s[2:3]
	v_sub_u32_e32 v9, v182, v5
	v_cmp_lt_i32_e64 s[2:3], s14, v5
	v_add_u32_e32 v5, 50, v4
	v_cmp_gt_u32_e32 vcc, s1, v9
	v_sub_u32_e32 v9, v182, v5
	s_and_b64 s[66:67], vcc, s[2:3]
	v_cmp_gt_u32_e32 vcc, s1, v9
	v_cmp_lt_i32_e64 s[2:3], s14, v5
	v_add_u32_e32 v5, 51, v4
	s_and_b64 s[68:69], vcc, s[2:3]
	v_sub_u32_e32 v9, v182, v5
	v_cmp_lt_i32_e64 s[2:3], s14, v5
	v_add_u32_e32 v5, 64, v4
	v_cmp_gt_u32_e32 vcc, s1, v9
	v_sub_u32_e32 v9, v182, v5
	s_and_b64 s[70:71], vcc, s[2:3]
	v_cmp_gt_u32_e32 vcc, s1, v9
	v_cmp_lt_i32_e64 s[2:3], s14, v5
	v_add_u32_e32 v5, 0x41, v4
	s_and_b64 s[72:73], vcc, s[2:3]
	v_sub_u32_e32 v9, v182, v5
	v_cmp_lt_i32_e64 s[2:3], s14, v5
	v_add_u32_e32 v5, 0x42, v4
	v_cmp_gt_u32_e32 vcc, s1, v9
	v_sub_u32_e32 v9, v182, v5
	s_and_b64 s[74:75], vcc, s[2:3]
	v_cmp_gt_u32_e32 vcc, s1, v9
	v_cmp_lt_i32_e64 s[2:3], s14, v5
	v_add_u32_e32 v5, 0x43, v4
	s_and_b64 s[76:77], vcc, s[2:3]
	v_sub_u32_e32 v9, v182, v5
	v_cmp_lt_i32_e64 s[2:3], s14, v5
	v_add_u32_e32 v5, 0x50, v4
	v_cmp_gt_u32_e32 vcc, s1, v9
	v_sub_u32_e32 v9, v182, v5
	s_and_b64 s[78:79], vcc, s[2:3]
	v_cmp_gt_u32_e32 vcc, s1, v9
	v_cmp_lt_i32_e64 s[2:3], s14, v5
	v_add_u32_e32 v5, 0x51, v4
	s_and_b64 s[80:81], vcc, s[2:3]
	v_sub_u32_e32 v9, v182, v5
	v_cmp_lt_i32_e64 s[2:3], s14, v5
	v_add_u32_e32 v5, 0x52, v4
	v_cmp_gt_u32_e32 vcc, s1, v9
	v_sub_u32_e32 v9, v182, v5
	s_and_b64 s[82:83], vcc, s[2:3]
	v_cmp_gt_u32_e32 vcc, s1, v9
	v_cmp_lt_i32_e64 s[2:3], s14, v5
	v_add_u32_e32 v5, 0x53, v4
	s_and_b64 s[84:85], vcc, s[2:3]
	v_sub_u32_e32 v9, v182, v5
	v_cmp_lt_i32_e64 s[2:3], s14, v5
	v_add_u32_e32 v5, 0x60, v4
	v_cmp_gt_u32_e32 vcc, s1, v9
	v_sub_u32_e32 v9, v182, v5
	s_and_b64 s[86:87], vcc, s[2:3]
	v_cmp_gt_u32_e32 vcc, s1, v9
	v_cmp_lt_i32_e64 s[2:3], s14, v5
	v_add_u32_e32 v5, 0x61, v4
	s_and_b64 s[88:89], vcc, s[2:3]
	v_sub_u32_e32 v9, v182, v5
	v_cmp_lt_i32_e64 s[2:3], s14, v5
	v_add_u32_e32 v5, 0x62, v4
	v_cmp_gt_u32_e32 vcc, s1, v9
	v_sub_u32_e32 v9, v182, v5
	s_and_b64 s[90:91], vcc, s[2:3]
	v_cmp_gt_u32_e32 vcc, s1, v9
	v_cmp_lt_i32_e64 s[2:3], s14, v5
	v_add_u32_e32 v5, 0x63, v4
	s_and_b64 s[92:93], vcc, s[2:3]
	v_sub_u32_e32 v9, v182, v5
	v_cmp_lt_i32_e64 s[2:3], s14, v5
	v_add_u32_e32 v5, 0x70, v4
	v_cmp_gt_u32_e32 vcc, s1, v9
	v_sub_u32_e32 v9, v182, v5
	s_and_b64 s[94:95], vcc, s[2:3]
	v_cmp_gt_u32_e32 vcc, s1, v9
	v_cmp_lt_i32_e64 s[2:3], s14, v5
	v_add_u32_e32 v5, 0x71, v4
	s_and_b64 s[96:97], vcc, s[2:3]
	v_sub_u32_e32 v9, v182, v5
	v_cmp_lt_i32_e64 s[2:3], s14, v5
	v_add_u32_e32 v5, 0x72, v4
	v_cmp_gt_u32_e32 vcc, s1, v9
	v_sub_u32_e32 v9, v182, v5
	v_cmp_lt_i32_e64 s[4:5], s14, v5
; #define GAS __attribute__((address_space(1)))
; #define LAS __attribute__((address_space(3)))
; __device__ __forceinline__ void swa_phase(const Ctx& C, const bf16* PROJ, const float* sinks, bf16* YSWA) {
;     ...
;         for (int i = 0; i < 2; ++i) { const int task = C.tid + 512 * i, kk = 2 * (task >> 3), c8 = task & 7;
;             v4u va = {0u, 0u, 0u, 0u}, vb = {0u, 0u, 0u, 0u};
;             if (n > 0 || kk >= 128) { const bf16* vp = PROJ + (size_t)(tb - 128 + kk) * INW + C_VS + 64 * hk + 8 * c8; va = *(const GAS v4u*)vp; vb = *(const GAS v4u*)(vp + INW); }
;             LAS unsigned* dst = (LAS unsigned*)(vt + (8 * c8) * 264 + kk);
;             dst[0] = (va.x & 0xffffu) | (vb.x << 16); dst[132] = (va.x >> 16) | (vb.x & 0xffff0000u); dst[2 * 132] = (va.y & 0xffffu) | (vb.y << 16); dst[3 * 132] = (va.y >> 16) | (vb.y & 0xffff0000u);
;             dst[4 * 132] = (va.z & 0xffffu) | (vb.z << 16); dst[5 * 132] = (va.z >> 16) | (vb.z & 0xffff0000u); dst[6 * 132] = (va.w & 0xffffu) | (vb.w << 16); dst[7 * 132] = (va.w >> 16) | (vb.w & 0xffff0000u); }
;         bf16x8 kf[9][2], qf[3][2];
;         { const int q0_ = tb + 16 * w;
; #pragma unroll
;           for (int j = 0; j < 9; ++j) { const int krow = 16 * w - 128 + 16 * j + c16; int ktok = tb + krow; if (128 * n + krow < 0) ktok = b * SEQ;
;               const bf16* kp = PROJ + (size_t)ktok * INW + C_KS + 64 * hk + 8 * g4; kf[j][0] = *(const GAS bf16x8*)kp; kf[j][1] = *(const GAS bf16x8*)(kp + 32); }
; #pragma unroll
;           for (int g = 0; g < 3; ++g) { const bf16* qp = PROJ + (size_t)(q0_ + c16) * INW + C_QS + 64 * (3 * hk + g) + 8 * g4; qf[g][0] = *(const GAS bf16x8*)qp; qf[g][1] = *(const GAS bf16x8*)(qp + 32); } }
	v_add_u32_e32 v5, 0x73, v4
	s_and_b64 s[2:3], vcc, s[2:3]
	v_cmp_gt_u32_e32 vcc, s1, v9
	v_sub_u32_e32 v9, v182, v5
	s_and_b64 s[4:5], vcc, s[4:5]
	v_cmp_gt_u32_e32 vcc, s1, v9
	v_cmp_lt_i32_e64 s[6:7], s14, v5
	v_sub_u32_e32 v5, v3, v0
	v_add_u32_e32 v8, s16, v0
	s_and_b64 s[6:7], vcc, s[6:7]
	v_cmp_gt_u32_e32 vcc, s1, v5
	v_add_u32_e32 v5, 0x81, v4
	v_cmp_lt_i32_e64 s[8:9], s14, v8
	v_sub_u32_e32 v9, v182, v5
	v_cmp_lt_i32_e64 s[10:11], s14, v5
	v_add_u32_e32 v5, 0x82, v4
	s_and_b64 s[8:9], vcc, s[8:9]
	v_cmp_gt_u32_e32 vcc, s1, v9
	v_sub_u32_e32 v9, v182, v5
	v_add_u32_e32 v4, 0x83, v4
	s_and_b64 s[10:11], vcc, s[10:11]
	v_cmp_gt_u32_e32 vcc, s1, v9
	v_cmp_lt_i32_e64 s[12:13], s14, v5
	v_sub_u32_e32 v5, v182, v4
	s_and_b64 s[12:13], vcc, s[12:13]
	v_cmp_gt_u32_e32 vcc, s1, v5
	v_readlane_b32 s0, v254, 41
	v_cmp_lt_i32_e64 s[14:15], s14, v4
	v_lshlrev_b32_e32 v4, 3, v1
	v_ashrrev_i32_e32 v1, 31, v0
	v_readlane_b32 s1, v254, 42
	v_add_u32_e32 v183, s16, v3
	v_readlane_b32 s16, v254, 49
	v_lshl_add_u64 v[172:173], v[0:1], 1, s[0:1]
	s_movk_i32 s0, 0x210
	v_mad_u32_u24 v0, v3, s0, 0
	v_min_i32_e32 v1, 0xec, v8
	v_lshl_add_u32 v195, v1, 1, v0
	v_add_u32_e32 v1, 32, v8
	v_min_i32_e32 v1, 0xec, v1
	v_lshl_add_u32 v196, v1, 1, v0
	v_add_u32_e32 v1, 64, v8
	v_min_i32_e32 v1, 0xec, v1
	v_lshl_add_u32 v197, v1, 1, v0
	v_add_u32_e32 v1, 0x60, v8
	v_min_i32_e32 v1, 0xec, v1
	v_lshl_add_u32 v204, v1, 1, v0
	v_add_u32_e32 v1, 0x80, v8
	v_min_i32_e32 v1, 0xec, v1
	v_lshl_add_u32 v194, v8, 1, v0
	v_lshl_add_u32 v205, v1, 1, v0
	v_ashrrev_i32_e32 v0, 2, v203
	v_and_b32_e32 v206, -2, v0
	s_movk_i32 s1, 0x7f
	v_add_u32_e32 v3, 0x200, v203
	s_and_b64 s[14:15], vcc, s[14:15]
	v_cmp_lt_i32_e32 vcc, s1, v206
	v_readlane_b32 s17, v254, 50
	v_ashrrev_i32_e32 v3, 2, v3
	s_or_b64 s[18:19], s[16:17], vcc
	v_and_b32_e32 v209, -2, v3
	v_and_b32_e32 v0, 7, v203
	v_writelane_b32 v255, s18, 12
	s_movk_i32 s0, 0x1080
	v_cmp_lt_i32_e32 vcc, s1, v209
	v_writelane_b32 v255, s19, 13
	v_mad_u32_u24 v1, v0, s0, 0
	s_or_b64 s[0:1], s[16:17], vcc
	v_writelane_b32 v255, s0, 14
	v_add_u32_e32 v184, 0xffffff80, v183
	v_ashrrev_i32_e32 v5, 31, v4
	v_writelane_b32 v255, s1, 15
	v_readlane_b32 s0, v254, 39
	v_readlane_b32 s1, v254, 40
	v_readlane_b32 s16, v254, 51
	v_add_u32_e32 v187, 0xffffff90, v183
	v_lshl_add_u64 v[176:177], v[4:5], 1, s[0:1]
	v_cmp_gt_i32_e64 s[0:1], s16, v184
	v_readlane_b32 s18, v255, 2
	v_add_u32_e32 v188, 0xffffffa0, v183
	v_writelane_b32 v255, s0, 16
	v_add_u32_e32 v189, 0xffffffb0, v183
	v_subrev_u32_e32 v190, 64, v183
	v_writelane_b32 v255, s1, 17
	v_cmp_gt_i32_e64 s[0:1], s16, v187
	v_subrev_u32_e32 v191, 48, v183
	v_subrev_u32_e32 v192, 32, v183
	v_writelane_b32 v255, s0, 18
	v_add_u32_e32 v193, -16, v183
	v_lshlrev_b32_e32 v185, 2, v7
	v_writelane_b32 v255, s1, 19
	v_cmp_gt_i32_e64 s[0:1], s16, v188
	v_lshlrev_b32_e32 v186, 2, v6
	v_lshl_add_u32 v208, v206, 1, v1
	v_writelane_b32 v255, s0, 20
	v_lshl_add_u32 v220, v209, 1, v1
	v_lshlrev_b32_e32 v174, 3, v0
	v_writelane_b32 v255, s1, 21
	v_cmp_gt_i32_e64 s[0:1], s16, v189
	v_lshlrev_b64 v[178:179], 1, v[4:5]
	v_readlane_b32 s19, v254, 25
	v_writelane_b32 v255, s0, 22
	v_cmp_gt_i32_e64 s[24:25], s16, v190
	v_cmp_gt_i32_e64 s[28:29], s16, v192
	v_writelane_b32 v255, s1, 23
	v_cmp_gt_i32_e64 s[0:1], s16, v191
	v_cmp_gt_i32_e64 s[16:17], s16, v193
	v_lshrrev_b32_e32 v185, 2, v215
	v_and_b32_e32 v186, 15, v215
	v_sub_u32_e32 v185, v185, v186
	v_mul_i32_i24_e32 v185, 0x2400, v185
	v_and_b32_e32 v186, 3, v215
	v_lshl_add_u32 v185, v186, 4, v185
	v_lshrrev_b32_e32 v186, 4, v215
	v_lshlrev_b32_e32 v186, 4, v186
	v_sub_u32_e32 v185, v185, v186
	v_ashrrev_i32_e32 v186, 31, v185
	v_add_co_u32_e32 v178, vcc, v178, v185
	v_addc_co_u32_e32 v179, vcc, v179, v186, vcc
	v_add_co_u32_e32 v176, vcc, v176, v185
	v_addc_co_u32_e32 v177, vcc, v177, v186, vcc
	v_and_b32_e32 v185, 15, v215
	v_lshlrev_b32_e32 v185, 4, v185
	v_lshrrev_b32_e32 v186, 4, v215
	v_lshl_or_b32 v185, v186, 2, v185
	s_branch .LBB0_532
.LBB0_531:
	s_or_b64 exec, exec, s[26:27]
	s_waitcnt vmcnt(0)
	v_lshlrev_b32_e32 v0, 16, v4
	s_mov_b32 s22, 0xffff
	v_lshrrev_b32_e32 v1, 16, v8
	s_mov_b32 s23, 0xffff0000
	v_and_or_b32 v0, v8, s22, v0
	v_and_or_b32 v1, v4, s23, v1
	ds_write2_b32 v220, v0, v1 offset1:132
	v_lshlrev_b32_e32 v0, 16, v5
	v_lshrrev_b32_e32 v1, 16, v9
	v_and_or_b32 v0, v9, s22, v0
	v_and_or_b32 v1, v5, s23, v1
	v_add_u32_e32 v3, 0x400, v220
	ds_write2_b32 v3, v0, v1 offset0:8 offset1:140
	v_lshlrev_b32_e32 v0, 16, v6
	v_lshrrev_b32_e32 v1, 16, v10
	v_and_or_b32 v0, v10, s22, v0
	v_and_or_b32 v1, v6, s23, v1
	v_add_u32_e32 v3, 0x800, v220
	ds_write2_b32 v3, v0, v1 offset0:16 offset1:148
	v_lshlrev_b32_e32 v0, 16, v7
	v_lshrrev_b32_e32 v1, 16, v11
	v_and_or_b32 v0, v11, s22, v0
	v_and_or_b32 v1, v7, s23, v1
	v_add_u32_e32 v3, 0xc00, v220
	v_readlane_b32 s22, v255, 16
	ds_write2_b32 v3, v0, v1 offset0:24 offset1:156
	v_add_u32_e32 v0, s35, v184
	v_mov_b32_e32 v3, s21
	v_readlane_b32 s23, v255, 17
	s_lshl_b32 s30, s20, 1
	v_readlane_b32 s20, v255, 18
	v_cndmask_b32_e64 v4, v0, v3, s[22:23]
	v_readlane_b32 s22, v254, 39
	v_readlane_b32 s23, v254, 40
	v_add_u32_e32 v12, s35, v187
	v_readlane_b32 s21, v255, 19
	v_mov_b64_e32 v[0:1], s[22:23]
	s_movk_i32 s26, 0x2400
	v_cndmask_b32_e64 v12, v12, v3, s[20:21]
	v_mad_i64_i32 v[12:13], s[20:21], v12, s26, v[0:1]
	v_readlane_b32 s20, v255, 20
	v_add_u32_e32 v20, s35, v188
	v_readlane_b32 s21, v255, 21
	v_add_u32_e32 v28, s35, v189
	v_add_u32_e32 v36, s35, v190
	v_cndmask_b32_e64 v20, v20, v3, s[20:21]
	v_mad_i64_i32 v[20:21], s[20:21], v20, s26, v[0:1]
	v_readlane_b32 s20, v255, 22
	v_readlane_b32 s21, v255, 23
; #define GAS __attribute__((address_space(1)))
; __device__ __forceinline__ void swa_phase(const Ctx& C, const bf16* PROJ, const float* sinks, bf16* YSWA) {
;     ...
;           for (int j = 0; j < 9; ++j) { const int krow = 16 * w - 128 + 16 * j + c16; int ktok = tb + krow; if (128 * n + krow < 0) ktok = b * SEQ;
;               const bf16* kp = PROJ + (size_t)ktok * INW + C_KS + 64 * hk + 8 * g4; kf[j][0] = *(const GAS bf16x8*)kp; kf[j][1] = *(const GAS bf16x8*)(kp + 32); }
; #pragma unroll
;           for (int g = 0; g < 3; ++g) { const bf16* qp = PROJ + (size_t)(q0_ + c16) * INW + C_QS + 64 * (3 * hk + g) + 8 * g4; qf[g][0] = *(const GAS bf16x8*)qp; qf[g][1] = *(const GAS bf16x8*)(qp + 32); } }
;         __syncthreads();
	v_add_u32_e32 v44, s35, v191
	v_add_u32_e32 v52, s35, v192
	v_add_u32_e32 v56, s35, v193
	v_cndmask_b32_e64 v28, v28, v3, s[20:21]
	v_cndmask_b32_e64 v36, v36, v3, s[24:25]
	v_cndmask_b32_e64 v44, v44, v3, s[0:1]
	v_cndmask_b32_e64 v52, v52, v3, s[28:29]
	v_cndmask_b32_e64 v3, v56, v3, s[16:17]
	v_mad_i64_i32 v[56:57], s[20:21], v3, s26, v[0:1]
	v_add_u32_e32 v3, s35, v183
	v_mad_i64_i32 v[4:5], s[22:23], v4, s26, v[0:1]
	v_mad_i64_i32 v[28:29], s[20:21], v28, s26, v[0:1]
	v_mad_i64_i32 v[36:37], s[20:21], v36, s26, v[0:1]
	v_mad_i64_i32 v[44:45], s[20:21], v44, s26, v[0:1]
	v_mad_i64_i32 v[52:53], s[20:21], v52, s26, v[0:1]
	v_mad_i64_i32 v[0:1], s[20:21], v3, s26, v[0:1]
	v_lshl_add_u64 v[4:5], v[4:5], 0, s[30:31]
	v_lshl_add_u64 v[12:13], v[12:13], 0, s[30:31]
	v_lshl_add_u64 v[20:21], v[20:21], 0, s[30:31]
	v_lshl_add_u64 v[28:29], v[28:29], 0, s[30:31]
	v_lshl_add_u64 v[36:37], v[36:37], 0, s[30:31]
	v_lshl_add_u64 v[44:45], v[44:45], 0, s[30:31]
	v_lshl_add_u64 v[52:53], v[52:53], 0, s[30:31]
	v_lshl_add_u64 v[56:57], v[56:57], 0, s[30:31]
	v_lshl_add_u64 v[0:1], v[0:1], 0, s[30:31]
	v_lshl_add_u64 v[8:9], v[4:5], 0, v[178:179]
	v_lshl_add_u64 v[16:17], v[12:13], 0, v[178:179]
	v_lshl_add_u64 v[24:25], v[20:21], 0, v[178:179]
	v_lshl_add_u64 v[32:33], v[28:29], 0, v[178:179]
	v_lshl_add_u64 v[40:41], v[36:37], 0, v[178:179]
	v_lshl_add_u64 v[48:49], v[44:45], 0, v[178:179]
	v_lshl_add_u64 v[52:53], v[52:53], 0, v[178:179]
	v_lshl_add_u64 v[56:57], v[56:57], 0, v[178:179]
	v_lshl_add_u64 v[0:1], v[0:1], 0, v[178:179]
	v_add_u32_e32 v3, s35, v182
	global_load_dwordx4 v[4:7], v[8:9], off offset:3584
	s_nop 0
	global_load_dwordx4 v[8:11], v[8:9], off offset:3648
	s_nop 0
	global_load_dwordx4 v[12:15], v[16:17], off offset:3584
	s_nop 0
	global_load_dwordx4 v[16:19], v[16:17], off offset:3648
	s_nop 0
	global_load_dwordx4 v[20:23], v[24:25], off offset:3584
	s_nop 0
	global_load_dwordx4 v[24:27], v[24:25], off offset:3648
	s_nop 0
	global_load_dwordx4 v[28:31], v[32:33], off offset:3584
	s_nop 0
	global_load_dwordx4 v[32:35], v[32:33], off offset:3648
	s_nop 0
	global_load_dwordx4 v[36:39], v[40:41], off offset:3584
	s_nop 0
	global_load_dwordx4 v[40:43], v[40:41], off offset:3648
	s_nop 0
	global_load_dwordx4 v[44:47], v[48:49], off offset:3584
	s_nop 0
	global_load_dwordx4 v[48:51], v[48:49], off offset:3648
	s_nop 0
	global_load_dwordx4 v[60:63], v[52:53], off offset:3584
	s_nop 0
	global_load_dwordx4 v[52:55], v[52:53], off offset:3648
	s_nop 0
	global_load_dwordx4 v[64:67], v[56:57], off offset:3584
	s_nop 0
	global_load_dwordx4 v[56:59], v[56:57], off offset:3648
	s_nop 0
	global_load_dwordx4 v[72:75], v[0:1], off offset:3584
	global_load_dwordx4 v[68:71], v[0:1], off offset:3648
	v_mad_i64_i32 v[0:1], s[22:23], v3, s26, v[176:177]
	s_mul_i32 s30, s34, 0x180
	v_lshl_add_u64 v[76:77], v[0:1], 0, s[30:31]
	global_load_dwordx4 v[88:91], v[76:77], off offset:2048
	global_load_dwordx4 v[84:87], v[76:77], off offset:2112
	s_mul_i32 s20, s34, 3
	s_lshl_b32 s21, s20, 7
	s_add_i32 s26, s21, 0x80
	s_mov_b32 s27, s31
	s_add_i32 s34, s21, 0x100
	s_mov_b32 s35, s31
	s_lshl_b32 s20, s20, 2
	v_lshl_add_u64 v[76:77], v[0:1], 0, s[26:27]
	v_lshl_add_u64 v[0:1], v[0:1], 0, s[34:35]
	s_movk_i32 s21, 0x600
	v_mov_b32_e32 v221, s20
	global_load_dwordx4 v[168:171], v[76:77], off offset:2048
	global_load_dwordx4 v[164:167], v[76:77], off offset:2112
	global_load_dwordx4 v[80:83], v[0:1], off offset:2048
	s_nop 0
	global_load_dwordx4 v[76:79], v[0:1], off offset:2112
	s_waitcnt lgkmcnt(0)
	s_barrier
	v_mad_i64_i32 v[180:181], s[22:23], v3, s21, v[172:173]
	global_load_dword v3, v221, s[36:37]
	s_waitcnt vmcnt(0)
	ds_bpermute_b32 v4, v185, v4
	ds_bpermute_b32 v5, v185, v5
	ds_bpermute_b32 v6, v185, v6
	ds_bpermute_b32 v7, v185, v7
	ds_bpermute_b32 v8, v185, v8
	ds_bpermute_b32 v9, v185, v9
	ds_bpermute_b32 v10, v185, v10
	ds_bpermute_b32 v11, v185, v11
	ds_bpermute_b32 v12, v185, v12
	ds_bpermute_b32 v13, v185, v13
	ds_bpermute_b32 v14, v185, v14
	ds_bpermute_b32 v15, v185, v15
	ds_bpermute_b32 v16, v185, v16
	ds_bpermute_b32 v17, v185, v17
	ds_bpermute_b32 v18, v185, v18
	ds_bpermute_b32 v19, v185, v19
	ds_bpermute_b32 v20, v185, v20
	ds_bpermute_b32 v21, v185, v21
	ds_bpermute_b32 v22, v185, v22
	ds_bpermute_b32 v23, v185, v23
	ds_bpermute_b32 v24, v185, v24
	ds_bpermute_b32 v25, v185, v25
	ds_bpermute_b32 v26, v185, v26
	ds_bpermute_b32 v27, v185, v27
	ds_bpermute_b32 v28, v185, v28
	ds_bpermute_b32 v29, v185, v29
	ds_bpermute_b32 v30, v185, v30
	ds_bpermute_b32 v31, v185, v31
	ds_bpermute_b32 v32, v185, v32
	ds_bpermute_b32 v33, v185, v33
	ds_bpermute_b32 v34, v185, v34
	ds_bpermute_b32 v35, v185, v35
	ds_bpermute_b32 v36, v185, v36
	ds_bpermute_b32 v37, v185, v37
	ds_bpermute_b32 v38, v185, v38
	ds_bpermute_b32 v39, v185, v39
	ds_bpermute_b32 v40, v185, v40
	ds_bpermute_b32 v41, v185, v41
	ds_bpermute_b32 v42, v185, v42
	ds_bpermute_b32 v43, v185, v43
	ds_bpermute_b32 v44, v185, v44
	ds_bpermute_b32 v45, v185, v45
	ds_bpermute_b32 v46, v185, v46
	ds_bpermute_b32 v47, v185, v47
	ds_bpermute_b32 v48, v185, v48
	ds_bpermute_b32 v49, v185, v49
	ds_bpermute_b32 v50, v185, v50
	ds_bpermute_b32 v51, v185, v51
	ds_bpermute_b32 v60, v185, v60
	ds_bpermute_b32 v61, v185, v61
	ds_bpermute_b32 v62, v185, v62
	ds_bpermute_b32 v63, v185, v63
	ds_bpermute_b32 v52, v185, v52
	ds_bpermute_b32 v53, v185, v53
	ds_bpermute_b32 v54, v185, v54
	ds_bpermute_b32 v55, v185, v55
	ds_bpermute_b32 v64, v185, v64
	ds_bpermute_b32 v65, v185, v65
	ds_bpermute_b32 v66, v185, v66
	ds_bpermute_b32 v67, v185, v67
	ds_bpermute_b32 v56, v185, v56
	ds_bpermute_b32 v57, v185, v57
	ds_bpermute_b32 v58, v185, v58
	ds_bpermute_b32 v59, v185, v59
	ds_bpermute_b32 v72, v185, v72
	ds_bpermute_b32 v73, v185, v73
	ds_bpermute_b32 v74, v185, v74
	ds_bpermute_b32 v75, v185, v75
	ds_bpermute_b32 v68, v185, v68
	ds_bpermute_b32 v69, v185, v69
	ds_bpermute_b32 v70, v185, v70
	ds_bpermute_b32 v71, v185, v71
	ds_bpermute_b32 v88, v185, v88
	ds_bpermute_b32 v89, v185, v89
	ds_bpermute_b32 v90, v185, v90
	ds_bpermute_b32 v91, v185, v91
	ds_bpermute_b32 v84, v185, v84
	ds_bpermute_b32 v85, v185, v85
	ds_bpermute_b32 v86, v185, v86
	ds_bpermute_b32 v87, v185, v87
	ds_bpermute_b32 v168, v185, v168
	ds_bpermute_b32 v169, v185, v169
	ds_bpermute_b32 v170, v185, v170
	ds_bpermute_b32 v171, v185, v171
	ds_bpermute_b32 v164, v185, v164
	ds_bpermute_b32 v165, v185, v165
	ds_bpermute_b32 v166, v185, v166
	ds_bpermute_b32 v167, v185, v167
	ds_bpermute_b32 v80, v185, v80
	ds_bpermute_b32 v81, v185, v81
	ds_bpermute_b32 v82, v185, v82
	ds_bpermute_b32 v83, v185, v83
	ds_bpermute_b32 v76, v185, v76
	ds_bpermute_b32 v77, v185, v77
	ds_bpermute_b32 v78, v185, v78
	ds_bpermute_b32 v79, v185, v79
	s_waitcnt lgkmcnt(0)
; #define MFMA16(a, b, c) __builtin_amdgcn_mfma_f32_16x16x32_bf16(a, b, c, 0, 0, 0)
; __device__ __forceinline__ void swa_phase(const Ctx& C, const bf16* PROJ, const float* sinks, bf16* YSWA) {
;     ...
;         for (int g = 0; g < 3; ++g) {
;             const int h = 3 * hk + g; const float sink2 = sinks[h] * LOG2E;
;             const int q0 = tb + 16 * w;
;             f32x4 s[9];
; #pragma unroll
;             for (int j = 0; j < 9; ++j) { f32x4 a = {0.f, 0.f, 0.f, 0.f}; a = MFMA16(kf[j][0], qf[g][0], a); a = MFMA16(kf[j][1], qf[g][1], a); s[j] = a; }
;             const int qr = 16 * w + c16; float mx = -INFINITY;
; #pragma unroll
;             for (int j = 0; j < 9; ++j)
; #pragma unroll
;                 for (int r = 0; r < 4; ++r) { const int kr = 16 * w - 128 + 16 * j + 4 * g4 + r, diff = qr - kr; const bool ok = diff >= 0 && diff < 128 && (128 * n + kr) >= 0;
;                     s[j][r] = ok ? s[j][r] : -INFINITY; mx = fmaxf(mx, s[j][r]); }
;             mx = fmaxf(mx, __shfl_xor(mx, 16)); mx = fmaxf(mx, __shfl_xor(mx, 32)); mx = fmaxf(mx, sink2);
;             float sum = 0.f;
; #pragma unroll
;             for (int j = 0; j < 9; ++j)
; #pragma unroll
;                 for (int r = 0; r < 4; ++r) { const float e = __builtin_amdgcn_exp2f(s[j][r] - mx); s[j][r] = e; sum += e; }
;             sum += __shfl_xor(sum, 16); sum += __shfl_xor(sum, 32); sum += __builtin_amdgcn_exp2f(sink2 - mx);
	v_mfma_f32_16x16x32_bf16 v[92:95], v[4:7], v[88:91], 0
	s_mov_b32 s22, 0xff800000
	s_mov_b32 s23, 0x3fb8aa3b
	s_addk_i32 s18, 0x2000
	v_mfma_f32_16x16x32_bf16 v[96:99], v[12:15], v[88:91], 0
	s_waitcnt vmcnt(5)
	v_mfma_f32_16x16x32_bf16 v[92:95], v[8:11], v[84:87], v[92:95]
	v_mfma_f32_16x16x32_bf16 v[100:103], v[20:23], v[88:91], 0
	v_mfma_f32_16x16x32_bf16 v[104:107], v[28:31], v[88:91], 0
	s_nop 5
	v_cndmask_b32_e64 v0, v216, v92, s[40:41]
	v_cndmask_b32_e64 v1, v216, v93, s[42:43]
	v_mfma_f32_16x16x32_bf16 v[108:111], v[36:39], v[88:91], 0
	v_mfma_f32_16x16x32_bf16 v[112:115], v[44:47], v[88:91], 0
	v_mfma_f32_16x16x32_bf16 v[116:119], v[60:63], v[88:91], 0
	v_mfma_f32_16x16x32_bf16 v[120:123], v[64:67], v[88:91], 0
	v_mfma_f32_16x16x32_bf16 v[88:91], v[72:75], v[88:91], 0
	v_mfma_f32_16x16x32_bf16 v[96:99], v[16:19], v[84:87], v[96:99]
	v_mfma_f32_16x16x32_bf16 v[100:103], v[24:27], v[84:87], v[100:103]
	v_mfma_f32_16x16x32_bf16 v[104:107], v[32:35], v[84:87], v[104:107]
	s_nop 5
	v_cndmask_b32_e64 v92, v216, v97, s[50:51]
	v_cndmask_b32_e64 v93, v216, v98, s[52:53]
	v_cndmask_b32_e64 v97, v216, v102, s[60:61]
	v_mfma_f32_16x16x32_bf16 v[108:111], v[40:43], v[84:87], v[108:111]
	v_cndmask_b32_e64 v98, v216, v103, s[62:63]
	v_cndmask_b32_e64 v102, v216, v107, s[70:71]
	v_mfma_f32_16x16x32_bf16 v[112:115], v[48:51], v[84:87], v[112:115]
	v_mfma_f32_16x16x32_bf16 v[116:119], v[52:55], v[84:87], v[116:119]
	s_nop 3
	v_cndmask_b32_e64 v103, v216, v108, s[72:73]
	s_nop 1
	v_cndmask_b32_e64 v107, v216, v112, s[80:81]
	v_cndmask_b32_e64 v108, v216, v113, s[82:83]
	v_mfma_f32_16x16x32_bf16 v[120:123], v[56:59], v[84:87], v[120:123]
	v_mfma_f32_16x16x32_bf16 v[84:87], v[68:71], v[84:87], v[88:91]
	v_cndmask_b32_e64 v112, v216, v117, s[90:91]
	v_cndmask_b32_e64 v113, v216, v118, s[92:93]
	s_nop 4
	v_cndmask_b32_e64 v117, v216, v122, s[4:5]
	v_max3_f32 v88, v0, s22, v1
	v_cndmask_b32_e64 v89, v216, v94, s[44:45]
	v_cndmask_b32_e64 v90, v216, v95, s[46:47]
	v_max3_f32 v88, v88, v89, v90
	v_cndmask_b32_e64 v91, v216, v96, s[48:49]
	v_max3_f32 v88, v88, v91, v92
	v_cndmask_b32_e64 v94, v216, v99, s[54:55]
	v_max3_f32 v88, v88, v93, v94
	v_cndmask_b32_e64 v95, v216, v100, s[56:57]
	v_cndmask_b32_e64 v96, v216, v101, s[58:59]
	v_max3_f32 v88, v88, v95, v96
	v_max3_f32 v88, v88, v97, v98
	v_cndmask_b32_e64 v99, v216, v104, s[64:65]
	v_cndmask_b32_e64 v100, v216, v105, s[66:67]
	v_max3_f32 v88, v88, v99, v100
	v_cndmask_b32_e64 v101, v216, v106, s[68:69]
	v_max3_f32 v88, v88, v101, v102
	v_cndmask_b32_e64 v104, v216, v109, s[74:75]
	v_max3_f32 v88, v88, v103, v104
	v_cndmask_b32_e64 v105, v216, v110, s[76:77]
	v_cndmask_b32_e64 v106, v216, v111, s[78:79]
	v_max3_f32 v88, v88, v105, v106
	v_max3_f32 v88, v88, v107, v108
	v_cndmask_b32_e64 v109, v216, v114, s[84:85]
	v_cndmask_b32_e64 v110, v216, v115, s[86:87]
	v_max3_f32 v88, v88, v109, v110
	v_cndmask_b32_e64 v111, v216, v116, s[88:89]
	v_max3_f32 v88, v88, v111, v112
	v_cndmask_b32_e64 v114, v216, v119, s[94:95]
	v_max3_f32 v88, v88, v113, v114
	v_cndmask_b32_e64 v115, v216, v120, s[96:97]
	v_cndmask_b32_e64 v116, v216, v121, s[2:3]
	v_max3_f32 v88, v88, v115, v116
	v_cndmask_b32_e64 v118, v216, v123, s[6:7]
	v_max3_f32 v88, v88, v117, v118
	v_cndmask_b32_e64 v119, v216, v84, s[8:9]
	v_cndmask_b32_e64 v120, v216, v85, s[10:11]
	v_max3_f32 v84, v88, v119, v120
	v_cndmask_b32_e64 v121, v216, v86, s[12:13]
	v_cndmask_b32_e64 v122, v216, v87, s[14:15]
	v_max3_f32 v84, v84, v121, v122
	v_mov_b32_e32 v86, v84
	s_nop 1
	v_permlane16_swap_b32_e32 v86, v84
	s_waitcnt vmcnt(0)
	v_mul_f32_e32 v85, 0x3fb8aa3b, v3
	v_mfma_f32_16x16x32_bf16 v[242:245], v[44:47], v[168:171], 0
	s_waitcnt lgkmcnt(0)
	v_max_f32_e32 v86, v86, v86
	v_max_f32_e32 v84, v84, v86
	v_mov_b32_e32 v86, v84
	s_nop 1
	v_permlane32_swap_b32_e32 v86, v84
	v_mfma_f32_16x16x32_bf16 v[246:249], v[60:63], v[168:171], 0
	s_waitcnt lgkmcnt(0)
	v_max3_f32 v123, v84, v86, v85
	v_sub_f32_e32 v88, v93, v123
	v_sub_f32_e32 v93, v98, v123
	v_sub_f32_e32 v98, v103, v123
	v_sub_f32_e32 v103, v108, v123
	v_sub_f32_e32 v108, v113, v123
	v_sub_f32_e32 v87, v92, v123
	v_sub_f32_e32 v92, v97, v123
	v_sub_f32_e32 v97, v102, v123
	v_sub_f32_e32 v102, v107, v123
	v_sub_f32_e32 v107, v112, v123
	v_exp_f32_e32 v112, v108
	v_sub_f32_e32 v108, v114, v123
	v_exp_f32_e32 v113, v108
	v_sub_f32_e32 v108, v115, v123
	v_exp_f32_e32 v114, v108
	v_sub_f32_e32 v108, v116, v123
	v_exp_f32_e32 v115, v108
	v_sub_f32_e32 v108, v117, v123
	v_sub_f32_e32 v0, v0, v123
	v_exp_f32_e32 v116, v108
	v_sub_f32_e32 v108, v118, v123
	v_exp_f32_e32 v0, v0
	v_sub_f32_e32 v1, v1, v123
	v_exp_f32_e32 v117, v108
	v_sub_f32_e32 v108, v119, v123
	v_exp_f32_e32 v1, v1
	v_sub_f32_e32 v84, v89, v123
	v_exp_f32_e32 v118, v108
	v_sub_f32_e32 v108, v120, v123
	v_exp_f32_e32 v84, v84
	v_sub_f32_e32 v85, v90, v123
	v_exp_f32_e32 v119, v108
	v_sub_f32_e32 v108, v121, v123
	v_exp_f32_e32 v85, v85
	v_sub_f32_e32 v86, v91, v123
	v_exp_f32_e32 v120, v108
	v_sub_f32_e32 v108, v122, v123
	v_exp_f32_e32 v86, v86
	v_exp_f32_e32 v121, v108
	v_add_f32_e32 v108, 0, v0
	v_exp_f32_e32 v87, v87
	v_add_f32_e32 v108, v1, v108
	v_exp_f32_e32 v88, v88
	v_sub_f32_e32 v89, v94, v123
	v_add_f32_e32 v108, v84, v108
	v_exp_f32_e32 v89, v89
	v_sub_f32_e32 v90, v95, v123
	v_add_f32_e32 v108, v85, v108
	v_exp_f32_e32 v90, v90
	v_sub_f32_e32 v91, v96, v123
	v_add_f32_e32 v108, v86, v108
	v_exp_f32_e32 v91, v91
	v_add_f32_e32 v108, v87, v108
	v_exp_f32_e32 v92, v92
	v_add_f32_e32 v108, v88, v108
	v_exp_f32_e32 v93, v93
	v_sub_f32_e32 v94, v99, v123
	v_add_f32_e32 v108, v89, v108
	v_exp_f32_e32 v94, v94
	v_sub_f32_e32 v95, v100, v123
; #define LAS __attribute__((address_space(3)))
; __device__ __forceinline__ unsigned pk2(float lo, float hi) { f32x2_m v = {lo, hi}; bf16x2_m b = __builtin_convertvector(v, bf16x2_m); return __builtin_bit_cast(unsigned, b); }
; #define MFMA16(a, b, c) __builtin_amdgcn_mfma_f32_16x16x32_bf16(a, b, c, 0, 0, 0)
; __device__ __forceinline__ void swa_phase(const Ctx& C, const bf16* PROJ, const float* sinks, bf16* YSWA) {
;     ...
;             sum += __shfl_xor(sum, 16); sum += __shfl_xor(sum, 32); sum += __builtin_amdgcn_exp2f(sink2 - mx);
;             const float inv = 1.0f / sum;
;             unsigned pw[10][2];
; #pragma unroll
;             for (int j = 0; j < 9; ++j) { pw[j][0] = pk2(s[j][0] * inv, s[j][1] * inv); pw[j][1] = pk2(s[j][2] * inv, s[j][3] * inv); }
;             pw[9][0] = 0u; pw[9][1] = 0u;
;             f32x4 o[4];
; #pragma unroll
;             for (int dt = 0; dt < 4; ++dt) o[dt] = (f32x4){0.f, 0.f, 0.f, 0.f};
; #pragma unroll
;             for (int sI = 0; sI < 5; ++sI) {
;                 const v4u pb = {pw[2 * sI][0], pw[2 * sI][1], pw[2 * sI + 1][0], pw[2 * sI + 1][1]};
;                 const int kkA = 16 * w + 32 * sI + 4 * g4; int kkB = kkA + 16; if (kkB > 252) kkB = 252;
; #pragma unroll
;                 for (int dt = 0; dt < 4; ++dt) { const LAS bf16* vp = vt + (16 * dt + c16) * 264;
;                     const v2u va = *(const LAS v2u*)(vp + kkA), vb = *(const LAS v2u*)(vp + kkB);
;                     const v4u av = {va.x, va.y, vb.x, vb.y};
;                     o[dt] = MFMA16(__builtin_bit_cast(bf16x8, av), __builtin_bit_cast(bf16x8, pb), o[dt]); }
;             }
	v_add_f32_e32 v108, v90, v108
	v_exp_f32_e32 v95, v95
	v_sub_f32_e32 v96, v101, v123
	v_add_f32_e32 v108, v91, v108
	v_exp_f32_e32 v96, v96
	v_add_f32_e32 v108, v92, v108
	v_exp_f32_e32 v97, v97
	v_add_f32_e32 v108, v93, v108
	v_exp_f32_e32 v98, v98
	v_sub_f32_e32 v99, v104, v123
	v_add_f32_e32 v108, v94, v108
	v_exp_f32_e32 v99, v99
	v_sub_f32_e32 v100, v105, v123
	v_add_f32_e32 v108, v95, v108
	v_exp_f32_e32 v100, v100
	v_sub_f32_e32 v101, v106, v123
	v_add_f32_e32 v108, v96, v108
	v_exp_f32_e32 v101, v101
	v_add_f32_e32 v108, v97, v108
	v_exp_f32_e32 v102, v102
	v_add_f32_e32 v108, v98, v108
	v_exp_f32_e32 v103, v103
	v_sub_f32_e32 v104, v109, v123
	v_add_f32_e32 v108, v99, v108
	v_exp_f32_e32 v104, v104
	v_sub_f32_e32 v105, v110, v123
	v_add_f32_e32 v108, v100, v108
	v_exp_f32_e32 v105, v105
	v_sub_f32_e32 v106, v111, v123
	v_add_f32_e32 v108, v101, v108
	v_exp_f32_e32 v106, v106
	v_add_f32_e32 v108, v102, v108
	v_exp_f32_e32 v107, v107
	v_add_f32_e32 v108, v103, v108
	v_add_f32_e32 v108, v104, v108
	v_add_f32_e32 v108, v105, v108
	v_add_f32_e32 v108, v106, v108
	v_add_f32_e32 v108, v107, v108
	v_add_f32_e32 v108, v112, v108
	v_add_f32_e32 v108, v113, v108
	v_add_f32_e32 v108, v114, v108
	v_add_f32_e32 v108, v115, v108
	v_add_f32_e32 v108, v116, v108
	v_add_f32_e32 v108, v117, v108
	v_add_f32_e32 v108, v118, v108
	v_add_f32_e32 v108, v119, v108
	v_add_f32_e32 v108, v120, v108
	v_add_f32_e32 v108, v121, v108
	v_mov_b32_e32 v109, v108
	s_nop 1
	v_permlane16_swap_b32_e32 v109, v108
	v_fma_f32 v3, v3, s23, -v123
	v_exp_f32_e32 v3, v3
	v_mfma_f32_16x16x32_bf16 v[242:245], v[48:51], v[164:167], v[242:245]
	s_waitcnt lgkmcnt(0)
	v_add_f32_e32 v108, v108, v109
	v_mov_b32_e32 v109, v108
	s_nop 1
	v_permlane32_swap_b32_e32 v109, v108
	v_mfma_f32_16x16x32_bf16 v[246:249], v[52:55], v[164:167], v[246:249]
	s_waitcnt lgkmcnt(0)
	v_add_f32_e32 v108, v108, v109
	v_add_f32_e32 v3, v3, v108
	v_div_scale_f32 v108, s[20:21], v3, v3, 1.0
	v_rcp_f32_e32 v109, v108
	s_nop 0
	v_fma_f32 v110, -v108, v109, 1.0
	v_fmac_f32_e32 v109, v110, v109
	v_div_scale_f32 v110, vcc, 1.0, v3, 1.0
	v_mul_f32_e32 v111, v110, v109
	v_fma_f32 v122, -v108, v111, v110
	v_fmac_f32_e32 v111, v122, v109
	v_fma_f32 v108, -v108, v111, v110
	v_div_fmas_f32 v108, v108, v109, v111
	v_div_fixup_f32 v122, v108, v3, 1.0
	v_pk_mul_f32 v[0:1], v[0:1], v[122:123] op_sel_hi:[1,0]
	v_add_u32_e32 v3, 0x100, v194
	v_cvt_pk_bf16_f32 v108, v0, v1
	v_pk_mul_f32 v[0:1], v[84:85], v[122:123] op_sel_hi:[1,0]
	v_pk_mul_f32 v[84:85], v[120:121], v[122:123] op_sel_hi:[1,0]
	v_cvt_pk_bf16_f32 v109, v0, v1
	v_pk_mul_f32 v[0:1], v[86:87], v[122:123] op_sel_hi:[1,0]
	s_nop 0
	v_cvt_pk_bf16_f32 v110, v0, v1
	v_pk_mul_f32 v[0:1], v[88:89], v[122:123] op_sel_hi:[1,0]
	s_nop 0
	v_cvt_pk_bf16_f32 v111, v0, v1
	v_pk_mul_f32 v[0:1], v[90:91], v[122:123] op_sel_hi:[1,0]
	s_nop 0
	v_cvt_pk_bf16_f32 v124, v0, v1
	v_pk_mul_f32 v[0:1], v[92:93], v[122:123] op_sel_hi:[1,0]
	s_nop 0
	v_cvt_pk_bf16_f32 v125, v0, v1
	v_pk_mul_f32 v[0:1], v[94:95], v[122:123] op_sel_hi:[1,0]
	s_nop 0
	v_cvt_pk_bf16_f32 v126, v0, v1
	v_pk_mul_f32 v[0:1], v[96:97], v[122:123] op_sel_hi:[1,0]
	s_nop 0
	v_cvt_pk_bf16_f32 v127, v0, v1
	v_pk_mul_f32 v[0:1], v[98:99], v[122:123] op_sel_hi:[1,0]
	s_nop 0
	v_cvt_pk_bf16_f32 v140, v0, v1
	v_pk_mul_f32 v[0:1], v[100:101], v[122:123] op_sel_hi:[1,0]
	s_nop 0
	v_cvt_pk_bf16_f32 v141, v0, v1
	v_pk_mul_f32 v[0:1], v[102:103], v[122:123] op_sel_hi:[1,0]
	s_nop 0
	v_cvt_pk_bf16_f32 v142, v0, v1
	v_pk_mul_f32 v[0:1], v[104:105], v[122:123] op_sel_hi:[1,0]
	s_nop 0
	v_cvt_pk_bf16_f32 v143, v0, v1
	v_pk_mul_f32 v[0:1], v[106:107], v[122:123] op_sel_hi:[1,0]
	s_nop 0
	v_cvt_pk_bf16_f32 v156, v0, v1
	v_pk_mul_f32 v[0:1], v[112:113], v[122:123] op_sel_hi:[1,0]
	s_nop 0
	v_cvt_pk_bf16_f32 v157, v0, v1
	v_pk_mul_f32 v[0:1], v[114:115], v[122:123] op_sel_hi:[1,0]
	ds_read2_b64 v[112:115], v194 offset1:8
	ds_read_b64 v[94:95], v195 offset:32
	v_cvt_pk_bf16_f32 v158, v0, v1
	v_pk_mul_f32 v[0:1], v[116:117], v[122:123] op_sel_hi:[1,0]
	s_waitcnt lgkmcnt(1)
	v_mov_b32_e32 v92, v112
	v_cvt_pk_bf16_f32 v159, v0, v1
	v_pk_mul_f32 v[0:1], v[118:119], v[122:123] op_sel_hi:[1,0]
	v_mov_b32_e32 v93, v113
	v_cvt_pk_bf16_f32 v0, v0, v1
	v_cvt_pk_bf16_f32 v1, v84, v85
	ds_read2st64_b64 v[84:87], v3 offset1:16
	ds_read_b64 v[98:99], v195 offset:8480
	s_waitcnt lgkmcnt(2)
	v_mfma_f32_16x16x32_bf16 v[116:119], v[92:95], v[108:111], 0
	s_waitcnt lgkmcnt(1)
	v_mov_b32_e32 v96, v86
	v_add_u32_e32 v86, 0x4000, v194
	ds_read2_b64 v[128:131], v86 offset0:64 offset1:72
	ds_read_b64 v[102:103], v195 offset:16928
	ds_read2st64_b64 v[88:91], v3 offset0:33 offset1:49
	ds_read_b64 v[106:107], v195 offset:25376
	v_mov_b32_e32 v97, v87
	v_add_u32_e32 v3, 0x2000, v194
	s_waitcnt lgkmcnt(3)
	v_mov_b32_e32 v100, v128
	v_mov_b32_e32 v101, v129
	s_waitcnt lgkmcnt(1)
	v_mov_b32_e32 v104, v90
	v_mov_b32_e32 v105, v91
	v_mfma_f32_16x16x32_bf16 v[120:123], v[96:99], v[108:111], 0
	v_add_u32_e32 v87, 0x6000, v194
	v_mfma_f32_16x16x32_bf16 v[132:135], v[100:103], v[108:111], 0
	s_waitcnt lgkmcnt(0)
	v_mfma_f32_16x16x32_bf16 v[136:139], v[104:107], v[108:111], 0
	ds_read_b64 v[110:111], v196 offset:32
	v_mov_b32_e32 v108, v114
	v_mov_b32_e32 v109, v115
	ds_read2_b64 v[148:151], v3 offset0:40 offset1:48
	ds_read_b64 v[114:115], v196 offset:8480
	s_waitcnt lgkmcnt(2)
	v_mfma_f32_16x16x32_bf16 v[144:147], v[108:111], v[124:127], v[116:119]
	s_waitcnt lgkmcnt(1)
	v_mov_b32_e32 v112, v148
	v_mov_b32_e32 v113, v149
	ds_read_b64 v[118:119], v196 offset:16928
	v_mov_b32_e32 v116, v130
	s_waitcnt lgkmcnt(1)
; #define GAS __attribute__((address_space(1)))
; #define LAS __attribute__((address_space(3)))
; __device__ __forceinline__ unsigned pk2(float lo, float hi) { f32x2_m v = {lo, hi}; bf16x2_m b = __builtin_convertvector(v, bf16x2_m); return __builtin_bit_cast(unsigned, b); }
; #define MFMA16(a, b, c) __builtin_amdgcn_mfma_f32_16x16x32_bf16(a, b, c, 0, 0, 0)
; __device__ __forceinline__ void swa_phase(const Ctx& C, const bf16* PROJ, const float* sinks, bf16* YSWA) {
;     ...
;         for (int g = 0; g < 3; ++g) {
;             const int h = 3 * hk + g; const float sink2 = sinks[h] * LOG2E;
;             const int q0 = tb + 16 * w;
;             f32x4 s[9];
; #pragma unroll
;             for (int j = 0; j < 9; ++j) { f32x4 a = {0.f, 0.f, 0.f, 0.f}; a = MFMA16(kf[j][0], qf[g][0], a); a = MFMA16(kf[j][1], qf[g][1], a); s[j] = a; }
;             const int qr = 16 * w + c16; float mx = -INFINITY;
; #pragma unroll
;             for (int j = 0; j < 9; ++j)
; #pragma unroll
;                 for (int r = 0; r < 4; ++r) { const int kr = 16 * w - 128 + 16 * j + 4 * g4 + r, diff = qr - kr; const bool ok = diff >= 0 && diff < 128 && (128 * n + kr) >= 0;
;                     s[j][r] = ok ? s[j][r] : -INFINITY; mx = fmaxf(mx, s[j][r]); }
;             mx = fmaxf(mx, __shfl_xor(mx, 16)); mx = fmaxf(mx, __shfl_xor(mx, 32)); mx = fmaxf(mx, sink2);
;     ...
;             f32x4 o[4];
; #pragma unroll
;             for (int dt = 0; dt < 4; ++dt) o[dt] = (f32x4){0.f, 0.f, 0.f, 0.f};
; #pragma unroll
;             for (int sI = 0; sI < 5; ++sI) {
;                 const v4u pb = {pw[2 * sI][0], pw[2 * sI][1], pw[2 * sI + 1][0], pw[2 * sI + 1][1]};
;                 const int kkA = 16 * w + 32 * sI + 4 * g4; int kkB = kkA + 16; if (kkB > 252) kkB = 252;
; #pragma unroll
;                 for (int dt = 0; dt < 4; ++dt) { const LAS bf16* vp = vt + (16 * dt + c16) * 264;
;                     const v2u va = *(const LAS v2u*)(vp + kkA), vb = *(const LAS v2u*)(vp + kkB);
;                     const v4u av = {va.x, va.y, vb.x, vb.y};
;                     o[dt] = MFMA16(__builtin_bit_cast(bf16x8, av), __builtin_bit_cast(bf16x8, pb), o[dt]); }
;             }
;             bf16* op = YSWA + (size_t)(q0 + c16) * 768 + 64 * h + 4 * g4;
; #pragma unroll
;             for (int dt = 0; dt < 4; ++dt) { v2u wv; wv.x = pk2(o[dt][0], o[dt][1]); wv.y = pk2(o[dt][2], o[dt][3]); *(GAS v2u*)(op + 16 * dt) = wv; }
	v_mfma_f32_16x16x32_bf16 v[152:155], v[112:115], v[124:127], v[120:123]
	ds_read2_b64 v[222:225], v87 offset0:104 offset1:112
	s_nop 1
	ds_read_b64 v[122:123], v196 offset:25376
	v_mov_b32_e32 v117, v131
	v_mov_b32_e32 v128, v150
	v_mov_b32_e32 v129, v151
	s_waitcnt lgkmcnt(1)
	v_mov_b32_e32 v120, v222
	v_mov_b32_e32 v121, v223
	v_mfma_f32_16x16x32_bf16 v[160:163], v[116:119], v[124:127], v[132:135]
	s_waitcnt lgkmcnt(0)
	v_mfma_f32_16x16x32_bf16 v[226:229], v[120:123], v[124:127], v[136:139]
	ds_read2_b64 v[230:233], v194 offset0:16 offset1:24
	ds_read_b64 v[126:127], v197 offset:32
	ds_read_b64 v[130:131], v197 offset:8480
	v_mov_b32_e32 v136, v224
	s_waitcnt lgkmcnt(0)
	v_mfma_f32_16x16x32_bf16 v[148:151], v[128:131], v[140:143], v[152:155]
	s_nop 2
	ds_read2_b64 v[152:155], v86 offset0:80 offset1:88
	ds_read_b64 v[134:135], v197 offset:16928
	ds_read_b64 v[138:139], v197 offset:25376
	v_mov_b32_e32 v124, v230
	v_mov_b32_e32 v125, v231
	s_waitcnt lgkmcnt(2)
	v_mov_b32_e32 v132, v152
	v_mov_b32_e32 v133, v153
	v_mov_b32_e32 v137, v225
	v_mfma_f32_16x16x32_bf16 v[144:147], v[124:127], v[140:143], v[144:147]
	s_waitcnt lgkmcnt(1)
	v_mfma_f32_16x16x32_bf16 v[160:163], v[132:135], v[140:143], v[160:163]
	s_waitcnt lgkmcnt(0)
	v_mfma_f32_16x16x32_bf16 v[222:225], v[136:139], v[140:143], v[226:229]
	ds_read_b64 v[142:143], v204 offset:32
	v_mov_b32_e32 v140, v232
	v_mov_b32_e32 v141, v233
	s_waitcnt lgkmcnt(0)
	s_nop 0
	v_mfma_f32_16x16x32_bf16 v[226:229], v[140:143], v[156:159], v[144:147]
	ds_read2_b64 v[230:233], v3 offset0:56 offset1:64
	s_nop 1
	ds_read_b64 v[146:147], v204 offset:8480
	v_mov_b32_e32 v3, v2
	s_waitcnt lgkmcnt(1)
	v_mov_b32_e32 v144, v230
	v_mov_b32_e32 v145, v231
	s_waitcnt lgkmcnt(0)
	s_nop 0
	v_mfma_f32_16x16x32_bf16 v[234:237], v[144:147], v[156:159], v[148:151]
	s_nop 2
	ds_read_b64 v[150:151], v204 offset:16928
	v_mov_b32_e32 v148, v154
	v_mov_b32_e32 v149, v155
	ds_read2_b64 v[238:241], v87 offset0:120 offset1:128
	ds_read_b64 v[154:155], v204 offset:25376
	s_waitcnt lgkmcnt(2)
	v_mfma_f32_16x16x32_bf16 v[160:163], v[148:151], v[156:159], v[160:163]
	s_waitcnt lgkmcnt(1)
	v_mov_b32_e32 v152, v238
	v_mov_b32_e32 v153, v239
	ds_read_b64 v[86:87], v205 offset:32
	ds_read_b64 v[90:91], v205 offset:16928
	s_waitcnt lgkmcnt(2)
	v_mfma_f32_16x16x32_bf16 v[222:225], v[152:155], v[156:159], v[222:225]
	ds_read_b64 v[158:159], v205 offset:8480
	v_mov_b32_e32 v156, v232
	v_mov_b32_e32 v157, v233
	s_waitcnt lgkmcnt(2)
	v_mfma_f32_16x16x32_bf16 v[226:229], v[84:87], v[0:3], v[226:229]
	s_waitcnt lgkmcnt(0)
	v_mfma_f32_16x16x32_bf16 v[230:233], v[156:159], v[0:3], v[234:237]
	s_nop 5
	v_cvt_pk_bf16_f32 v198, v226, v227
	v_cvt_pk_bf16_f32 v199, v228, v229
	v_mfma_f32_16x16x32_bf16 v[234:237], v[88:91], v[0:3], v[160:163]
	s_nop 2
	ds_read_b64 v[162:163], v205 offset:25376
	v_mov_b32_e32 v160, v240
	v_mov_b32_e32 v161, v241
	v_mfma_f32_16x16x32_bf16 v[226:229], v[12:15], v[168:171], 0
	s_waitcnt lgkmcnt(0)
	v_mfma_f32_16x16x32_bf16 v[222:225], v[160:163], v[0:3], v[222:225]
	v_lshl_add_u64 v[0:1], v[180:181], 0, s[30:31]
	global_store_dwordx2 v[0:1], v[198:199], off
	v_cvt_pk_bf16_f32 v198, v230, v231
	v_cvt_pk_bf16_f32 v199, v232, v233
	global_store_dwordx2 v[0:1], v[198:199], off offset:32
	v_cvt_pk_bf16_f32 v198, v234, v235
	v_cvt_pk_bf16_f32 v199, v236, v237
	global_store_dwordx2 v[0:1], v[198:199], off offset:64
	v_cvt_pk_bf16_f32 v198, v222, v223
	v_cvt_pk_bf16_f32 v199, v224, v225
	global_store_dwordx2 v[0:1], v[198:199], off offset:96
	global_load_dword v3, v221, s[36:37] offset:4
	v_mfma_f32_16x16x32_bf16 v[222:225], v[4:7], v[168:171], 0
	v_mfma_f32_16x16x32_bf16 v[222:225], v[8:11], v[164:167], v[222:225]
	v_mfma_f32_16x16x32_bf16 v[230:233], v[20:23], v[168:171], 0
	v_mfma_f32_16x16x32_bf16 v[234:237], v[28:31], v[168:171], 0
	s_nop 5
	v_cndmask_b32_e64 v0, v216, v222, s[40:41]
	v_cndmask_b32_e64 v1, v216, v223, s[42:43]
	v_mfma_f32_16x16x32_bf16 v[238:241], v[36:39], v[168:171], 0
	v_mfma_f32_16x16x32_bf16 v[198:201], v[64:67], v[168:171], 0
	v_mfma_f32_16x16x32_bf16 v[168:171], v[72:75], v[168:171], 0
	v_mfma_f32_16x16x32_bf16 v[226:229], v[16:19], v[164:167], v[226:229]
	v_mfma_f32_16x16x32_bf16 v[230:233], v[24:27], v[164:167], v[230:233]
	v_mfma_f32_16x16x32_bf16 v[234:237], v[32:35], v[164:167], v[234:237]
	s_nop 5
	v_cndmask_b32_e64 v222, v216, v227, s[50:51]
	v_cndmask_b32_e64 v223, v216, v228, s[52:53]
	v_cndmask_b32_e64 v227, v216, v232, s[60:61]
	v_mfma_f32_16x16x32_bf16 v[238:241], v[40:43], v[164:167], v[238:241]
	v_cndmask_b32_e64 v228, v216, v233, s[62:63]
	v_cndmask_b32_e64 v232, v216, v237, s[70:71]
	v_cndmask_b32_e64 v237, v216, v242, s[80:81]
	v_mfma_f32_16x16x32_bf16 v[198:201], v[56:59], v[164:167], v[198:201]
	v_cndmask_b32_e64 v242, v216, v247, s[90:91]
	s_nop 2
	v_cndmask_b32_e64 v233, v216, v238, s[72:73]
	v_cndmask_b32_e64 v238, v216, v243, s[82:83]
	v_mfma_f32_16x16x32_bf16 v[164:167], v[68:71], v[164:167], v[168:171]
	v_cndmask_b32_e64 v243, v216, v248, s[92:93]
	v_cndmask_b32_e64 v247, v216, v200, s[4:5]
	v_cndmask_b32_e64 v248, v216, v201, s[6:7]
	v_max3_f32 v168, v0, s22, v1
	v_cndmask_b32_e64 v169, v216, v224, s[44:45]
	v_cndmask_b32_e64 v170, v216, v225, s[46:47]
	v_max3_f32 v168, v168, v169, v170
	v_cndmask_b32_e64 v171, v216, v226, s[48:49]
	v_max3_f32 v168, v168, v171, v222
	v_cndmask_b32_e64 v224, v216, v229, s[54:55]
	v_max3_f32 v168, v168, v223, v224
	v_cndmask_b32_e64 v225, v216, v230, s[56:57]
	v_cndmask_b32_e64 v226, v216, v231, s[58:59]
	v_max3_f32 v168, v168, v225, v226
	v_max3_f32 v168, v168, v227, v228
	v_cndmask_b32_e64 v229, v216, v234, s[64:65]
	v_cndmask_b32_e64 v230, v216, v235, s[66:67]
	v_max3_f32 v168, v168, v229, v230
	v_cndmask_b32_e64 v231, v216, v236, s[68:69]
	v_max3_f32 v168, v168, v231, v232
	v_cndmask_b32_e64 v234, v216, v239, s[74:75]
	v_max3_f32 v168, v168, v233, v234
	v_cndmask_b32_e64 v235, v216, v240, s[76:77]
	v_cndmask_b32_e64 v236, v216, v241, s[78:79]
	v_max3_f32 v168, v168, v235, v236
	v_max3_f32 v168, v168, v237, v238
	v_cndmask_b32_e64 v239, v216, v244, s[84:85]
	v_cndmask_b32_e64 v240, v216, v245, s[86:87]
	v_max3_f32 v168, v168, v239, v240
	v_cndmask_b32_e64 v241, v216, v246, s[88:89]
	v_max3_f32 v168, v168, v241, v242
	v_cndmask_b32_e64 v244, v216, v249, s[94:95]
	v_max3_f32 v168, v168, v243, v244
	v_cndmask_b32_e64 v245, v216, v198, s[96:97]
	v_cndmask_b32_e64 v246, v216, v199, s[2:3]
	v_max3_f32 v168, v168, v245, v246
	v_max3_f32 v168, v168, v247, v248
	v_cndmask_b32_e64 v249, v216, v164, s[8:9]
	v_cndmask_b32_e64 v252, v216, v165, s[10:11]
	v_max3_f32 v164, v168, v249, v252
	v_cndmask_b32_e64 v168, v216, v166, s[12:13]
	v_cndmask_b32_e64 v217, v216, v167, s[14:15]
	v_max3_f32 v164, v164, v168, v217
	v_mov_b32_e32 v166, v164
	s_nop 1
	v_permlane16_swap_b32_e32 v166, v164
	s_waitcnt vmcnt(0)
; __device__ __forceinline__ unsigned pk2(float lo, float hi) { f32x2_m v = {lo, hi}; bf16x2_m b = __builtin_convertvector(v, bf16x2_m); return __builtin_bit_cast(unsigned, b); }
; __device__ __forceinline__ void swa_phase(const Ctx& C, const bf16* PROJ, const float* sinks, bf16* YSWA) {
;     ...
;             mx = fmaxf(mx, __shfl_xor(mx, 16)); mx = fmaxf(mx, __shfl_xor(mx, 32)); mx = fmaxf(mx, sink2);
;             float sum = 0.f;
; #pragma unroll
;             for (int j = 0; j < 9; ++j)
; #pragma unroll
;                 for (int r = 0; r < 4; ++r) { const float e = __builtin_amdgcn_exp2f(s[j][r] - mx); s[j][r] = e; sum += e; }
;             sum += __shfl_xor(sum, 16); sum += __shfl_xor(sum, 32); sum += __builtin_amdgcn_exp2f(sink2 - mx);
;             const float inv = 1.0f / sum;
;             unsigned pw[10][2];
; #pragma unroll
;             for (int j = 0; j < 9; ++j) { pw[j][0] = pk2(s[j][0] * inv, s[j][1] * inv); pw[j][1] = pk2(s[j][2] * inv, s[j][3] * inv); }
	v_mul_f32_e32 v165, 0x3fb8aa3b, v3
	v_mfma_f32_16x16x32_bf16 v[4:7], v[4:7], v[80:83], 0
	s_waitcnt lgkmcnt(0)
	v_max_f32_e32 v166, v166, v166
	v_max_f32_e32 v164, v164, v166
	v_mov_b32_e32 v166, v164
	s_nop 1
	v_permlane32_swap_b32_e32 v166, v164
	v_mfma_f32_16x16x32_bf16 v[4:7], v[8:11], v[76:79], v[4:7]
	s_waitcnt lgkmcnt(0)
	v_max3_f32 v207, v164, v166, v165
	v_sub_f32_e32 v164, v169, v207
	v_sub_f32_e32 v169, v223, v207
	v_exp_f32_e32 v198, v169
	v_sub_f32_e32 v169, v224, v207
	v_exp_f32_e32 v199, v169
	v_sub_f32_e32 v169, v225, v207
	v_exp_f32_e32 v200, v169
	v_sub_f32_e32 v169, v226, v207
	v_exp_f32_e32 v201, v169
	v_sub_f32_e32 v169, v227, v207
	v_sub_f32_e32 v167, v222, v207
	v_exp_f32_e32 v222, v169
	v_sub_f32_e32 v169, v228, v207
	v_exp_f32_e32 v223, v169
	v_sub_f32_e32 v169, v229, v207
	v_exp_f32_e32 v224, v169
	v_sub_f32_e32 v169, v230, v207
	v_exp_f32_e32 v225, v169
	v_sub_f32_e32 v169, v231, v207
	v_exp_f32_e32 v226, v169
	v_sub_f32_e32 v169, v232, v207
	v_exp_f32_e32 v227, v169
	v_sub_f32_e32 v169, v233, v207
	v_exp_f32_e32 v228, v169
	v_sub_f32_e32 v169, v234, v207
	v_exp_f32_e32 v229, v169
	v_sub_f32_e32 v169, v235, v207
	v_exp_f32_e32 v230, v169
	v_sub_f32_e32 v169, v236, v207
	v_exp_f32_e32 v231, v169
	v_sub_f32_e32 v169, v237, v207
	v_exp_f32_e32 v232, v169
	v_sub_f32_e32 v169, v238, v207
	v_exp_f32_e32 v233, v169
	v_sub_f32_e32 v169, v239, v207
	v_exp_f32_e32 v234, v169
	v_sub_f32_e32 v169, v240, v207
	v_exp_f32_e32 v235, v169
	v_sub_f32_e32 v169, v241, v207
	v_sub_f32_e32 v0, v0, v207
	v_exp_f32_e32 v236, v169
	v_sub_f32_e32 v169, v242, v207
	v_exp_f32_e32 v0, v0
	v_sub_f32_e32 v1, v1, v207
	v_exp_f32_e32 v237, v169
	v_sub_f32_e32 v169, v243, v207
	v_exp_f32_e32 v1, v1
	v_exp_f32_e32 v238, v169
	v_sub_f32_e32 v169, v244, v207
	v_exp_f32_e32 v164, v164
	v_sub_f32_e32 v165, v170, v207
	v_exp_f32_e32 v239, v169
	v_sub_f32_e32 v169, v245, v207
	v_sub_f32_e32 v168, v168, v207
	v_exp_f32_e32 v165, v165
	v_sub_f32_e32 v166, v171, v207
	v_exp_f32_e32 v240, v169
	v_sub_f32_e32 v169, v246, v207
	v_exp_f32_e32 v246, v168
	v_sub_f32_e32 v168, v217, v207
	v_exp_f32_e32 v166, v166
	v_exp_f32_e32 v241, v169
	v_sub_f32_e32 v169, v247, v207
	v_exp_f32_e32 v247, v168
	v_add_f32_e32 v168, 0, v0
	v_exp_f32_e32 v167, v167
	v_add_f32_e32 v168, v1, v168
	v_add_f32_e32 v168, v164, v168
	v_add_f32_e32 v168, v165, v168
	v_add_f32_e32 v168, v166, v168
	v_add_f32_e32 v168, v167, v168
	v_add_f32_e32 v168, v198, v168
	v_add_f32_e32 v168, v199, v168
	v_add_f32_e32 v168, v200, v168
	v_add_f32_e32 v168, v201, v168
	v_add_f32_e32 v168, v222, v168
	v_add_f32_e32 v168, v223, v168
	v_add_f32_e32 v168, v224, v168
	v_add_f32_e32 v168, v225, v168
	v_add_f32_e32 v168, v226, v168
	v_add_f32_e32 v168, v227, v168
	v_add_f32_e32 v168, v228, v168
	v_add_f32_e32 v168, v229, v168
	v_add_f32_e32 v168, v230, v168
	v_add_f32_e32 v168, v231, v168
	v_add_f32_e32 v168, v232, v168
	v_add_f32_e32 v168, v233, v168
	v_add_f32_e32 v168, v234, v168
	v_add_f32_e32 v168, v235, v168
	v_add_f32_e32 v168, v236, v168
	v_add_f32_e32 v168, v237, v168
	v_exp_f32_e32 v242, v169
	v_sub_f32_e32 v169, v248, v207
	v_add_f32_e32 v168, v238, v168
	v_exp_f32_e32 v243, v169
	v_sub_f32_e32 v169, v249, v207
	v_add_f32_e32 v168, v239, v168
	v_exp_f32_e32 v244, v169
	v_sub_f32_e32 v169, v252, v207
	v_add_f32_e32 v168, v240, v168
	v_exp_f32_e32 v245, v169
	v_add_f32_e32 v168, v241, v168
	v_add_f32_e32 v168, v242, v168
	v_add_f32_e32 v168, v243, v168
	v_add_f32_e32 v168, v244, v168
	v_add_f32_e32 v168, v245, v168
	v_add_f32_e32 v168, v246, v168
	v_add_f32_e32 v168, v247, v168
	v_mov_b32_e32 v169, v168
	s_nop 1
	v_permlane16_swap_b32_e32 v169, v168
	v_fma_f32 v3, v3, s23, -v207
	v_exp_f32_e32 v3, v3
	v_mfma_f32_16x16x32_bf16 v[8:11], v[12:15], v[80:83], 0
	s_waitcnt lgkmcnt(0)
	v_add_f32_e32 v168, v168, v169
	v_mov_b32_e32 v169, v168
	s_nop 1
	v_permlane32_swap_b32_e32 v169, v168
	v_mfma_f32_16x16x32_bf16 v[12:15], v[20:23], v[80:83], 0
	s_waitcnt lgkmcnt(0)
	v_add_f32_e32 v168, v168, v169
	v_add_f32_e32 v3, v3, v168
	v_div_scale_f32 v168, s[20:21], v3, v3, 1.0
	v_rcp_f32_e32 v169, v168
	v_mfma_f32_16x16x32_bf16 v[8:11], v[16:19], v[76:79], v[8:11]
	v_fma_f32 v170, -v168, v169, 1.0
	v_fmac_f32_e32 v169, v170, v169
	v_div_scale_f32 v170, vcc, 1.0, v3, 1.0
	v_mul_f32_e32 v171, v170, v169
	v_fma_f32 v207, -v168, v171, v170
	v_fmac_f32_e32 v171, v207, v169
	v_fma_f32 v168, -v168, v171, v170
	v_div_fmas_f32 v168, v168, v169, v171
	v_div_fixup_f32 v248, v168, v3, 1.0
	v_pk_mul_f32 v[0:1], v[0:1], v[248:249] op_sel_hi:[1,0]
	v_mov_b32_e32 v3, v2
	v_cvt_pk_bf16_f32 v168, v0, v1
	v_pk_mul_f32 v[0:1], v[164:165], v[248:249] op_sel_hi:[1,0]
	v_mfma_f32_16x16x32_bf16 v[16:19], v[28:31], v[80:83], 0
	v_cvt_pk_bf16_f32 v169, v0, v1
	v_pk_mul_f32 v[0:1], v[166:167], v[248:249] op_sel_hi:[1,0]
	s_nop 0
	v_cvt_pk_bf16_f32 v170, v0, v1
	v_pk_mul_f32 v[0:1], v[198:199], v[248:249] op_sel_hi:[1,0]
	v_mfma_f32_16x16x32_bf16 v[12:15], v[24:27], v[76:79], v[12:15]
	v_cvt_pk_bf16_f32 v171, v0, v1
	v_pk_mul_f32 v[0:1], v[200:201], v[248:249] op_sel_hi:[1,0]
	s_nop 0
	v_cvt_pk_bf16_f32 v198, v0, v1
	v_pk_mul_f32 v[0:1], v[222:223], v[248:249] op_sel_hi:[1,0]
	v_mfma_f32_16x16x32_bf16 v[20:23], v[36:39], v[80:83], 0
	v_cvt_pk_bf16_f32 v199, v0, v1
	v_pk_mul_f32 v[0:1], v[224:225], v[248:249] op_sel_hi:[1,0]
	s_nop 0
	v_cvt_pk_bf16_f32 v200, v0, v1
	v_pk_mul_f32 v[0:1], v[226:227], v[248:249] op_sel_hi:[1,0]
	v_pk_mul_f32 v[226:227], v[246:247], v[248:249] op_sel_hi:[1,0]
	v_cvt_pk_bf16_f32 v201, v0, v1
	v_pk_mul_f32 v[0:1], v[228:229], v[248:249] op_sel_hi:[1,0]
	v_mfma_f32_16x16x32_bf16 v[16:19], v[32:35], v[76:79], v[16:19]
; #define GAS __attribute__((address_space(1)))
; #define LAS __attribute__((address_space(3)))
; __device__ __forceinline__ unsigned pk2(float lo, float hi) { f32x2_m v = {lo, hi}; bf16x2_m b = __builtin_convertvector(v, bf16x2_m); return __builtin_bit_cast(unsigned, b); }
; #define MFMA16(a, b, c) __builtin_amdgcn_mfma_f32_16x16x32_bf16(a, b, c, 0, 0, 0)
; __device__ __forceinline__ void swa_phase(const Ctx& C, const bf16* PROJ, const float* sinks, bf16* YSWA) {
;     ...
;             for (int j = 0; j < 9; ++j) { f32x4 a = {0.f, 0.f, 0.f, 0.f}; a = MFMA16(kf[j][0], qf[g][0], a); a = MFMA16(kf[j][1], qf[g][1], a); s[j] = a; }
;             const int qr = 16 * w + c16; float mx = -INFINITY;
; #pragma unroll
;             for (int j = 0; j < 9; ++j)
; #pragma unroll
;                 for (int r = 0; r < 4; ++r) { const int kr = 16 * w - 128 + 16 * j + 4 * g4 + r, diff = qr - kr; const bool ok = diff >= 0 && diff < 128 && (128 * n + kr) >= 0;
;                     s[j][r] = ok ? s[j][r] : -INFINITY; mx = fmaxf(mx, s[j][r]); }
;             mx = fmaxf(mx, __shfl_xor(mx, 16)); mx = fmaxf(mx, __shfl_xor(mx, 32)); mx = fmaxf(mx, sink2);
;     ...
;             f32x4 o[4];
; #pragma unroll
;             for (int dt = 0; dt < 4; ++dt) o[dt] = (f32x4){0.f, 0.f, 0.f, 0.f};
; #pragma unroll
;             for (int sI = 0; sI < 5; ++sI) {
;                 const v4u pb = {pw[2 * sI][0], pw[2 * sI][1], pw[2 * sI + 1][0], pw[2 * sI + 1][1]};
;                 const int kkA = 16 * w + 32 * sI + 4 * g4; int kkB = kkA + 16; if (kkB > 252) kkB = 252;
; #pragma unroll
;                 for (int dt = 0; dt < 4; ++dt) { const LAS bf16* vp = vt + (16 * dt + c16) * 264;
;                     const v2u va = *(const LAS v2u*)(vp + kkA), vb = *(const LAS v2u*)(vp + kkB);
;                     const v4u av = {va.x, va.y, vb.x, vb.y};
;                     o[dt] = MFMA16(__builtin_bit_cast(bf16x8, av), __builtin_bit_cast(bf16x8, pb), o[dt]); }
;             }
;             bf16* op = YSWA + (size_t)(q0 + c16) * 768 + 64 * h + 4 * g4;
; #pragma unroll
;             for (int dt = 0; dt < 4; ++dt) { v2u wv; wv.x = pk2(o[dt][0], o[dt][1]); wv.y = pk2(o[dt][2], o[dt][3]); *(GAS v2u*)(op + 16 * dt) = wv; }
	v_cvt_pk_bf16_f32 v222, v0, v1
	v_pk_mul_f32 v[0:1], v[230:231], v[248:249] op_sel_hi:[1,0]
	s_nop 0
	v_cvt_pk_bf16_f32 v223, v0, v1
	v_pk_mul_f32 v[0:1], v[232:233], v[248:249] op_sel_hi:[1,0]
	v_mfma_f32_16x16x32_bf16 v[230:233], v[96:99], v[168:171], 0
	v_cvt_pk_bf16_f32 v224, v0, v1
	v_pk_mul_f32 v[0:1], v[234:235], v[248:249] op_sel_hi:[1,0]
	s_nop 0
	v_cvt_pk_bf16_f32 v225, v0, v1
	v_pk_mul_f32 v[0:1], v[236:237], v[248:249] op_sel_hi:[1,0]
	v_mfma_f32_16x16x32_bf16 v[234:237], v[100:103], v[168:171], 0
	v_cvt_pk_bf16_f32 v164, v0, v1
	v_pk_mul_f32 v[0:1], v[238:239], v[248:249] op_sel_hi:[1,0]
	s_nop 0
	v_cvt_pk_bf16_f32 v165, v0, v1
	v_pk_mul_f32 v[0:1], v[240:241], v[248:249] op_sel_hi:[1,0]
	v_mfma_f32_16x16x32_bf16 v[230:233], v[112:115], v[198:201], v[230:233]
	v_cvt_pk_bf16_f32 v166, v0, v1
	v_pk_mul_f32 v[0:1], v[242:243], v[248:249] op_sel_hi:[1,0]
	s_nop 0
	v_cvt_pk_bf16_f32 v167, v0, v1
	v_pk_mul_f32 v[0:1], v[244:245], v[248:249] op_sel_hi:[1,0]
	v_mfma_f32_16x16x32_bf16 v[234:237], v[116:119], v[198:201], v[234:237]
	v_cvt_pk_bf16_f32 v0, v0, v1
	v_cvt_pk_bf16_f32 v1, v226, v227
	v_mfma_f32_16x16x32_bf16 v[226:229], v[92:95], v[168:171], 0
	v_mfma_f32_16x16x32_bf16 v[168:171], v[104:107], v[168:171], 0
	v_mfma_f32_16x16x32_bf16 v[226:229], v[108:111], v[198:201], v[226:229]
	v_mfma_f32_16x16x32_bf16 v[168:171], v[120:123], v[198:201], v[168:171]
	v_mfma_f32_16x16x32_bf16 v[198:201], v[124:127], v[222:225], v[226:229]
	v_mfma_f32_16x16x32_bf16 v[226:229], v[128:131], v[222:225], v[230:233]
	v_mfma_f32_16x16x32_bf16 v[230:233], v[132:135], v[222:225], v[234:237]
	v_mfma_f32_16x16x32_bf16 v[168:171], v[136:139], v[222:225], v[168:171]
	v_mfma_f32_16x16x32_bf16 v[198:201], v[140:143], v[164:167], v[198:201]
	v_mfma_f32_16x16x32_bf16 v[222:225], v[144:147], v[164:167], v[226:229]
	v_mfma_f32_16x16x32_bf16 v[226:229], v[148:151], v[164:167], v[230:233]
	v_mfma_f32_16x16x32_bf16 v[164:167], v[152:155], v[164:167], v[168:171]
	v_mfma_f32_16x16x32_bf16 v[168:171], v[84:87], v[0:3], v[198:201]
	v_mfma_f32_16x16x32_bf16 v[198:201], v[156:159], v[0:3], v[222:225]
	v_mfma_f32_16x16x32_bf16 v[222:225], v[88:91], v[0:3], v[226:229]
	s_nop 5
	v_cvt_pk_bf16_f32 v168, v168, v169
	v_cvt_pk_bf16_f32 v169, v170, v171
	v_mfma_f32_16x16x32_bf16 v[164:167], v[160:163], v[0:3], v[164:167]
	v_lshl_add_u64 v[0:1], v[180:181], 0, s[26:27]
	global_store_dwordx2 v[0:1], v[168:169], off
	v_cvt_pk_bf16_f32 v168, v198, v199
	v_cvt_pk_bf16_f32 v169, v200, v201
	global_store_dwordx2 v[0:1], v[168:169], off offset:32
	v_cvt_pk_bf16_f32 v168, v222, v223
	v_cvt_pk_bf16_f32 v169, v224, v225
	s_nop 0
	v_cvt_pk_bf16_f32 v164, v164, v165
	v_cvt_pk_bf16_f32 v165, v166, v167
	global_store_dwordx2 v[0:1], v[168:169], off offset:64
	global_store_dwordx2 v[0:1], v[164:165], off offset:96
	global_load_dword v3, v221, s[36:37] offset:8
	v_cndmask_b32_e64 v0, v216, v4, s[40:41]
	v_cndmask_b32_e64 v1, v216, v5, s[42:43]
	v_max3_f32 v4, v0, s22, v1
	v_cndmask_b32_e64 v5, v216, v6, s[44:45]
	v_cndmask_b32_e64 v6, v216, v7, s[46:47]
	v_mfma_f32_16x16x32_bf16 v[24:27], v[44:47], v[80:83], 0
	v_max3_f32 v4, v4, v5, v6
	v_cndmask_b32_e64 v7, v216, v8, s[48:49]
	v_cndmask_b32_e64 v8, v216, v9, s[50:51]
	v_max3_f32 v4, v4, v7, v8
	v_cndmask_b32_e64 v9, v216, v10, s[52:53]
	v_cndmask_b32_e64 v10, v216, v11, s[54:55]
	v_mfma_f32_16x16x32_bf16 v[20:23], v[40:43], v[76:79], v[20:23]
	v_max3_f32 v4, v4, v9, v10
	v_cndmask_b32_e64 v11, v216, v12, s[56:57]
	v_cndmask_b32_e64 v40, v216, v13, s[58:59]
	v_mfma_f32_16x16x32_bf16 v[28:31], v[60:63], v[80:83], 0
	v_max3_f32 v4, v4, v11, v40
	v_cndmask_b32_e64 v41, v216, v14, s[60:61]
	v_cndmask_b32_e64 v42, v216, v15, s[62:63]
	v_mfma_f32_16x16x32_bf16 v[24:27], v[48:51], v[76:79], v[24:27]
	v_max3_f32 v4, v4, v41, v42
	v_cndmask_b32_e64 v43, v216, v16, s[64:65]
	v_cndmask_b32_e64 v44, v216, v17, s[66:67]
	v_mfma_f32_16x16x32_bf16 v[32:35], v[64:67], v[80:83], 0
	v_max3_f32 v4, v4, v43, v44
	v_cndmask_b32_e64 v45, v216, v18, s[68:69]
	v_cndmask_b32_e64 v46, v216, v19, s[70:71]
	v_mfma_f32_16x16x32_bf16 v[28:31], v[52:55], v[76:79], v[28:31]
	v_max3_f32 v4, v4, v45, v46
	v_cndmask_b32_e64 v47, v216, v20, s[72:73]
	v_cndmask_b32_e64 v48, v216, v21, s[74:75]
	v_mfma_f32_16x16x32_bf16 v[36:39], v[72:75], v[80:83], 0
	v_max3_f32 v4, v4, v47, v48
	v_cndmask_b32_e64 v49, v216, v22, s[76:77]
	v_cndmask_b32_e64 v50, v216, v23, s[78:79]
	v_mfma_f32_16x16x32_bf16 v[32:35], v[56:59], v[76:79], v[32:35]
	v_max3_f32 v4, v4, v49, v50
	v_cndmask_b32_e64 v51, v216, v24, s[80:81]
	v_cndmask_b32_e64 v52, v216, v25, s[82:83]
	v_max3_f32 v4, v4, v51, v52
	v_cndmask_b32_e64 v53, v216, v26, s[84:85]
	v_cndmask_b32_e64 v54, v216, v27, s[86:87]
	v_mfma_f32_16x16x32_bf16 v[36:39], v[68:71], v[76:79], v[36:39]
	v_max3_f32 v4, v4, v53, v54
	v_cndmask_b32_e64 v55, v216, v28, s[88:89]
	v_cndmask_b32_e64 v56, v216, v29, s[90:91]
	v_max3_f32 v4, v4, v55, v56
	v_cndmask_b32_e64 v57, v216, v30, s[92:93]
	v_cndmask_b32_e64 v58, v216, v31, s[94:95]
	v_max3_f32 v4, v4, v57, v58
	v_cndmask_b32_e64 v59, v216, v32, s[96:97]
	v_cndmask_b32_e64 v60, v216, v33, s[2:3]
	v_max3_f32 v4, v4, v59, v60
	v_cndmask_b32_e64 v61, v216, v34, s[4:5]
	v_cndmask_b32_e64 v62, v216, v35, s[6:7]
	v_max3_f32 v4, v4, v61, v62
	v_cndmask_b32_e64 v63, v216, v36, s[8:9]
	v_cndmask_b32_e64 v64, v216, v37, s[10:11]
	v_max3_f32 v4, v4, v63, v64
	v_cndmask_b32_e64 v65, v216, v38, s[12:13]
	v_cndmask_b32_e64 v66, v216, v39, s[14:15]
	v_max3_f32 v4, v4, v65, v66
	v_mov_b32_e32 v13, v4
	s_nop 1
	v_permlane16_swap_b32_e32 v13, v4
	s_waitcnt lgkmcnt(0)
; __device__ __forceinline__ void swa_phase(const Ctx& C, const bf16* PROJ, const float* sinks, bf16* YSWA) {
;     ...
;             mx = fmaxf(mx, __shfl_xor(mx, 16)); mx = fmaxf(mx, __shfl_xor(mx, 32)); mx = fmaxf(mx, sink2);
;             float sum = 0.f;
; #pragma unroll
;             for (int j = 0; j < 9; ++j)
; #pragma unroll
;                 for (int r = 0; r < 4; ++r) { const float e = __builtin_amdgcn_exp2f(s[j][r] - mx); s[j][r] = e; sum += e; }
;             sum += __shfl_xor(sum, 16); sum += __shfl_xor(sum, 32); sum += __builtin_amdgcn_exp2f(sink2 - mx);
	v_max_f32_e32 v13, v13, v13
	v_max_f32_e32 v4, v4, v13
	v_mov_b32_e32 v13, v4
	s_nop 1
	v_permlane32_swap_b32_e32 v13, v4
	s_waitcnt vmcnt(0)
	v_mul_f32_e32 v12, 0x3fb8aa3b, v3
	s_waitcnt lgkmcnt(0)
	v_max3_f32 v67, v4, v13, v12
	v_sub_f32_e32 v4, v5, v67
	v_sub_f32_e32 v5, v6, v67
	v_sub_f32_e32 v6, v7, v67
	v_sub_f32_e32 v7, v8, v67
	v_sub_f32_e32 v8, v9, v67
	v_exp_f32_e32 v12, v8
	v_sub_f32_e32 v8, v10, v67
	v_exp_f32_e32 v13, v8
	v_sub_f32_e32 v8, v11, v67
	v_exp_f32_e32 v14, v8
	v_sub_f32_e32 v8, v40, v67
	v_exp_f32_e32 v15, v8
	v_sub_f32_e32 v8, v41, v67
	v_exp_f32_e32 v16, v8
	v_sub_f32_e32 v8, v42, v67
	v_exp_f32_e32 v17, v8
	v_sub_f32_e32 v8, v43, v67
	v_exp_f32_e32 v18, v8
	v_sub_f32_e32 v8, v44, v67
	v_exp_f32_e32 v19, v8
	v_sub_f32_e32 v8, v45, v67
	v_exp_f32_e32 v20, v8
	v_sub_f32_e32 v8, v46, v67
	v_exp_f32_e32 v21, v8
	v_sub_f32_e32 v8, v47, v67
	v_exp_f32_e32 v22, v8
	v_sub_f32_e32 v8, v48, v67
	v_exp_f32_e32 v23, v8
	v_sub_f32_e32 v8, v49, v67
	v_exp_f32_e32 v24, v8
	v_sub_f32_e32 v8, v50, v67
	v_exp_f32_e32 v25, v8
	v_sub_f32_e32 v8, v51, v67
	v_exp_f32_e32 v26, v8
	v_sub_f32_e32 v8, v52, v67
	v_exp_f32_e32 v27, v8
	v_sub_f32_e32 v8, v53, v67
	v_exp_f32_e32 v28, v8
	v_sub_f32_e32 v8, v54, v67
	v_exp_f32_e32 v29, v8
	v_sub_f32_e32 v8, v55, v67
	v_exp_f32_e32 v30, v8
	v_sub_f32_e32 v8, v56, v67
	v_exp_f32_e32 v31, v8
	v_sub_f32_e32 v8, v57, v67
	v_exp_f32_e32 v32, v8
	v_sub_f32_e32 v8, v58, v67
	v_exp_f32_e32 v33, v8
	v_sub_f32_e32 v8, v59, v67
	v_exp_f32_e32 v34, v8
	v_sub_f32_e32 v8, v60, v67
	v_exp_f32_e32 v35, v8
	v_sub_f32_e32 v8, v61, v67
	v_sub_f32_e32 v0, v0, v67
	v_exp_f32_e32 v36, v8
	v_sub_f32_e32 v8, v62, v67
	v_exp_f32_e32 v0, v0
	v_sub_f32_e32 v1, v1, v67
	v_exp_f32_e32 v37, v8
	v_sub_f32_e32 v8, v63, v67
	v_exp_f32_e32 v1, v1
	v_exp_f32_e32 v38, v8
	v_sub_f32_e32 v8, v64, v67
	v_exp_f32_e32 v4, v4
	v_exp_f32_e32 v39, v8
	v_sub_f32_e32 v8, v65, v67
	v_exp_f32_e32 v5, v5
	v_exp_f32_e32 v40, v8
	v_sub_f32_e32 v8, v66, v67
	v_exp_f32_e32 v6, v6
	v_exp_f32_e32 v41, v8
	v_add_f32_e32 v8, 0, v0
	v_exp_f32_e32 v7, v7
	v_add_f32_e32 v8, v1, v8
	v_add_f32_e32 v8, v4, v8
	v_add_f32_e32 v8, v5, v8
	v_add_f32_e32 v8, v6, v8
	v_add_f32_e32 v8, v7, v8
	v_add_f32_e32 v8, v12, v8
	v_add_f32_e32 v8, v13, v8
	v_add_f32_e32 v8, v14, v8
	v_add_f32_e32 v8, v15, v8
	v_add_f32_e32 v8, v16, v8
	v_add_f32_e32 v8, v17, v8
	v_add_f32_e32 v8, v18, v8
	v_add_f32_e32 v8, v19, v8
	v_add_f32_e32 v8, v20, v8
	v_add_f32_e32 v8, v21, v8
	v_add_f32_e32 v8, v22, v8
	v_add_f32_e32 v8, v23, v8
	v_add_f32_e32 v8, v24, v8
	v_add_f32_e32 v8, v25, v8
	v_add_f32_e32 v8, v26, v8
	v_add_f32_e32 v8, v27, v8
	v_add_f32_e32 v8, v28, v8
	v_add_f32_e32 v8, v29, v8
	v_add_f32_e32 v8, v30, v8
	v_add_f32_e32 v8, v31, v8
	v_add_f32_e32 v8, v32, v8
	v_add_f32_e32 v8, v33, v8
	v_add_f32_e32 v8, v34, v8
	v_add_f32_e32 v8, v35, v8
	v_add_f32_e32 v8, v36, v8
	v_add_f32_e32 v8, v37, v8
	v_add_f32_e32 v8, v38, v8
	v_add_f32_e32 v8, v39, v8
	v_add_f32_e32 v8, v40, v8
	v_add_f32_e32 v8, v41, v8
	v_mov_b32_e32 v9, v8
	s_nop 1
	v_permlane16_swap_b32_e32 v9, v8
	v_fma_f32 v3, v3, s23, -v67
	v_exp_f32_e32 v3, v3
	s_waitcnt lgkmcnt(0)
	v_add_f32_e32 v8, v8, v9
	v_mov_b32_e32 v9, v8
	s_nop 1
	v_permlane32_swap_b32_e32 v9, v8
	s_waitcnt lgkmcnt(0)
; #define GAS __attribute__((address_space(1)))
; #define LAS __attribute__((address_space(3)))
; __device__ __forceinline__ unsigned pk2(float lo, float hi) { f32x2_m v = {lo, hi}; bf16x2_m b = __builtin_convertvector(v, bf16x2_m); return __builtin_bit_cast(unsigned, b); }
; #define MFMA16(a, b, c) __builtin_amdgcn_mfma_f32_16x16x32_bf16(a, b, c, 0, 0, 0)
; __device__ __forceinline__ void swa_phase(const Ctx& C, const bf16* PROJ, const float* sinks, bf16* YSWA) {
;     ...
;     for (int u = C.vcu; u < 512; u += C.G) {
;     ...
;             sum += __shfl_xor(sum, 16); sum += __shfl_xor(sum, 32); sum += __builtin_amdgcn_exp2f(sink2 - mx);
;             const float inv = 1.0f / sum;
;             unsigned pw[10][2];
; #pragma unroll
;             for (int j = 0; j < 9; ++j) { pw[j][0] = pk2(s[j][0] * inv, s[j][1] * inv); pw[j][1] = pk2(s[j][2] * inv, s[j][3] * inv); }
;             pw[9][0] = 0u; pw[9][1] = 0u;
;             f32x4 o[4];
; #pragma unroll
;             for (int dt = 0; dt < 4; ++dt) o[dt] = (f32x4){0.f, 0.f, 0.f, 0.f};
; #pragma unroll
;             for (int sI = 0; sI < 5; ++sI) {
;                 const v4u pb = {pw[2 * sI][0], pw[2 * sI][1], pw[2 * sI + 1][0], pw[2 * sI + 1][1]};
;                 const int kkA = 16 * w + 32 * sI + 4 * g4; int kkB = kkA + 16; if (kkB > 252) kkB = 252;
; #pragma unroll
;                 for (int dt = 0; dt < 4; ++dt) { const LAS bf16* vp = vt + (16 * dt + c16) * 264;
;                     const v2u va = *(const LAS v2u*)(vp + kkA), vb = *(const LAS v2u*)(vp + kkB);
;                     const v4u av = {va.x, va.y, vb.x, vb.y};
;                     o[dt] = MFMA16(__builtin_bit_cast(bf16x8, av), __builtin_bit_cast(bf16x8, pb), o[dt]); }
;             }
;             bf16* op = YSWA + (size_t)(q0 + c16) * 768 + 64 * h + 4 * g4;
; #pragma unroll
;             for (int dt = 0; dt < 4; ++dt) { v2u wv; wv.x = pk2(o[dt][0], o[dt][1]); wv.y = pk2(o[dt][2], o[dt][3]); *(GAS v2u*)(op + 16 * dt) = wv; }
	v_add_f32_e32 v8, v8, v9
	v_add_f32_e32 v3, v3, v8
	v_div_scale_f32 v8, s[20:21], v3, v3, 1.0
	v_rcp_f32_e32 v9, v8
	s_add_i32 s20, s19, 0x100
	s_cmpk_lt_i32 s19, 0x100
	s_mov_b32 s19, s20
	v_fma_f32 v10, -v8, v9, 1.0
	v_fmac_f32_e32 v9, v10, v9
	v_div_scale_f32 v10, vcc, 1.0, v3, 1.0
	v_mul_f32_e32 v11, v10, v9
	v_fma_f32 v42, -v8, v11, v10
	v_fmac_f32_e32 v11, v42, v9
	v_fma_f32 v8, -v8, v11, v10
	v_div_fmas_f32 v8, v8, v9, v11
	v_div_fixup_f32 v42, v8, v3, 1.0
	v_pk_mul_f32 v[0:1], v[0:1], v[42:43] op_sel_hi:[1,0]
	v_mov_b32_e32 v3, v2
	v_cvt_pk_bf16_f32 v8, v0, v1
	v_pk_mul_f32 v[0:1], v[4:5], v[42:43] op_sel_hi:[1,0]
	s_nop 0
	v_cvt_pk_bf16_f32 v9, v0, v1
	v_pk_mul_f32 v[0:1], v[6:7], v[42:43] op_sel_hi:[1,0]
	s_nop 0
	v_cvt_pk_bf16_f32 v10, v0, v1
	v_pk_mul_f32 v[0:1], v[12:13], v[42:43] op_sel_hi:[1,0]
	s_nop 0
	v_cvt_pk_bf16_f32 v11, v0, v1
	v_pk_mul_f32 v[0:1], v[14:15], v[42:43] op_sel_hi:[1,0]
	s_nop 0
	v_cvt_pk_bf16_f32 v12, v0, v1
	v_pk_mul_f32 v[0:1], v[16:17], v[42:43] op_sel_hi:[1,0]
	s_nop 0
	v_cvt_pk_bf16_f32 v13, v0, v1
	v_pk_mul_f32 v[0:1], v[18:19], v[42:43] op_sel_hi:[1,0]
	s_nop 0
	v_cvt_pk_bf16_f32 v14, v0, v1
	v_pk_mul_f32 v[0:1], v[20:21], v[42:43] op_sel_hi:[1,0]
	v_pk_mul_f32 v[20:21], v[40:41], v[42:43] op_sel_hi:[1,0]
	v_cvt_pk_bf16_f32 v15, v0, v1
	v_pk_mul_f32 v[0:1], v[22:23], v[42:43] op_sel_hi:[1,0]
	s_nop 0
	v_cvt_pk_bf16_f32 v16, v0, v1
	v_pk_mul_f32 v[0:1], v[24:25], v[42:43] op_sel_hi:[1,0]
	s_nop 0
	v_cvt_pk_bf16_f32 v17, v0, v1
	v_pk_mul_f32 v[0:1], v[26:27], v[42:43] op_sel_hi:[1,0]
	v_mfma_f32_16x16x32_bf16 v[24:27], v[96:99], v[8:11], 0
	v_cvt_pk_bf16_f32 v18, v0, v1
	v_pk_mul_f32 v[0:1], v[28:29], v[42:43] op_sel_hi:[1,0]
	s_nop 0
	v_cvt_pk_bf16_f32 v19, v0, v1
	v_pk_mul_f32 v[0:1], v[30:31], v[42:43] op_sel_hi:[1,0]
	v_mfma_f32_16x16x32_bf16 v[28:31], v[100:103], v[8:11], 0
	v_cvt_pk_bf16_f32 v4, v0, v1
	v_pk_mul_f32 v[0:1], v[32:33], v[42:43] op_sel_hi:[1,0]
	s_nop 0
	v_cvt_pk_bf16_f32 v5, v0, v1
	v_pk_mul_f32 v[0:1], v[34:35], v[42:43] op_sel_hi:[1,0]
	v_mfma_f32_16x16x32_bf16 v[24:27], v[112:115], v[12:15], v[24:27]
	v_cvt_pk_bf16_f32 v6, v0, v1
	v_pk_mul_f32 v[0:1], v[36:37], v[42:43] op_sel_hi:[1,0]
	s_nop 0
	v_cvt_pk_bf16_f32 v7, v0, v1
	v_pk_mul_f32 v[0:1], v[38:39], v[42:43] op_sel_hi:[1,0]
	v_mfma_f32_16x16x32_bf16 v[28:31], v[116:119], v[12:15], v[28:31]
	v_cvt_pk_bf16_f32 v0, v0, v1
	v_cvt_pk_bf16_f32 v1, v20, v21
	v_mfma_f32_16x16x32_bf16 v[20:23], v[92:95], v[8:11], 0
	v_mfma_f32_16x16x32_bf16 v[8:11], v[104:107], v[8:11], 0
	v_mfma_f32_16x16x32_bf16 v[20:23], v[108:111], v[12:15], v[20:23]
	v_mfma_f32_16x16x32_bf16 v[8:11], v[120:123], v[12:15], v[8:11]
	v_mfma_f32_16x16x32_bf16 v[12:15], v[124:127], v[16:19], v[20:23]
	v_mfma_f32_16x16x32_bf16 v[20:23], v[128:131], v[16:19], v[24:27]
	v_mfma_f32_16x16x32_bf16 v[24:27], v[132:135], v[16:19], v[28:31]
	v_mfma_f32_16x16x32_bf16 v[8:11], v[136:139], v[16:19], v[8:11]
	v_mfma_f32_16x16x32_bf16 v[12:15], v[140:143], v[4:7], v[12:15]
	v_mfma_f32_16x16x32_bf16 v[16:19], v[144:147], v[4:7], v[20:23]
	v_mfma_f32_16x16x32_bf16 v[20:23], v[148:151], v[4:7], v[24:27]
	v_mfma_f32_16x16x32_bf16 v[4:7], v[152:155], v[4:7], v[8:11]
	v_mfma_f32_16x16x32_bf16 v[8:11], v[84:87], v[0:3], v[12:15]
	v_mfma_f32_16x16x32_bf16 v[12:15], v[156:159], v[0:3], v[16:19]
	v_mfma_f32_16x16x32_bf16 v[16:19], v[88:91], v[0:3], v[20:23]
	s_nop 5
	v_cvt_pk_bf16_f32 v8, v8, v9
	v_cvt_pk_bf16_f32 v9, v10, v11
	v_mfma_f32_16x16x32_bf16 v[4:7], v[160:163], v[0:3], v[4:7]
	v_lshl_add_u64 v[0:1], v[180:181], 0, s[34:35]
	global_store_dwordx2 v[0:1], v[8:9], off
	v_cvt_pk_bf16_f32 v8, v12, v13
	v_cvt_pk_bf16_f32 v9, v14, v15
	global_store_dwordx2 v[0:1], v[8:9], off offset:32
	v_cvt_pk_bf16_f32 v8, v16, v17
	v_cvt_pk_bf16_f32 v9, v18, v19
	s_nop 0
	v_cvt_pk_bf16_f32 v4, v4, v5
	v_cvt_pk_bf16_f32 v5, v6, v7
	global_store_dwordx2 v[0:1], v[8:9], off offset:64
	global_store_dwordx2 v[0:1], v[4:5], off offset:96
	s_cbranch_scc0 .LBB0_536
